# hand-scheduled scan-wave loop (fewer VALU, full unroll, immediate LDS offsets) + XP5 96 (32 w_down items moved from scan phase to GU converters)
# speedup vs baseline: 1.0051x; 1.0051x over previous
; #define LAS __attribute__((address_space(3)))
; __device__ __forceinline__ void scan_head(const Params& p, LAS unsigned char* lds, int bh, const int wave) {
;     ...
;         if (wave < 4) {
;             __builtin_amdgcn_s_setprio(3);
;             const int bp = chunk & 1, vb = chunk % 3;
;             const LAS unsigned char* awp = lds + L_AW + bp * 8192 + sel * 128 + rg * 16;
;             const LAS unsigned char* wwp = lds + L_W + bp * 8192 + rg * 16;
;             const LAS unsigned char* abp = lds + L_BK + bp * 16384 + rg * 256 + ri * 4;
;             const LAS unsigned char* vp = lds + L_V + vb * 8192 + (16 * wave + ri) * 4;
;             const LAS unsigned char* csp = lds + L_CS + bp * 256;
;             LAS unsigned char* yp = (rg == 0) ? (lds + L_Y + bp * 8192 + (16 * wave + ri) * 4) : ((rg == 2) ? (lds + L_Y + bp * 8192 + 256 + (16 * wave + ri) * 4) : (lds + L_DUMMY + tid * 4));
;             const int y_st = (rg & 1) ? 0 : 512;
;     ...
;             bf16x8 Pa0, Pa1, Qa0, Qa1; f32x4 Pw0, Pw1, Pw2, Pw3, Qw0, Qw1, Qw2, Qw3, Pcs, Qcs; float Pb0, Pb1, Pb2, Pb3, Pvt, Pvu, Qb0, Qb1, Qb2, Qb3, Qvt, Qvu;
;             SCAN_LD(P, 0);
; #pragma unroll 1
;             for (int pi = 0; pi < 16; pi += 2) {
;                 SCAN_LD(Q, pi + 1);
;                 SCAN_STEP(P, pi);
;                 if (pi + 2 < 16) SCAN_LD(P, pi + 2);
;                 SCAN_STEP(Q, pi + 1);
;             }
.LBB0_806:
	s_and_b64 vcc, exec, s[14:15]
	s_cbranch_vccz .LBB0_789
	s_setprio 3
	s_and_b32 s2, s51, 1
	s_lshl_b32 s15, s2, 13
	s_mul_i32 s14, s51, 0xab
	s_lshl_b32 s52, s2, 14
	s_bfe_u32 s14, s14, 0x70009
	s_lshl_b32 s44, s2, 8
	s_mul_i32 s14, s14, 3
	s_waitcnt vmcnt(0)
	s_sub_i32 s14, s51, s14
	s_and_b32 s14, s14, 0xff
	s_lshl_b32 s14, s14, 13
	s_add_i32 s44, s44, 0x20300
	v_add_u32_e32 v98, s15, v176
	v_add_u32_e32 v99, s15, v175
	v_add_u32_e32 v0, s52, v178
	v_add_u32_e32 v1, s14, v179
	v_add_u32_e32 v0, 0x8000, v0
	v_add_u32_e32 v4, 0x100, v1
	v_mov_b32_e32 v2, s44
	v_cndmask_b32_e64 v4, v4, v1, s[8:9]
	v_cndmask_b32_e64 v4, v4, v1, s[12:13]
	v_cndmask_b32_e64 v1, v4, v1, s[10:11]
	v_add_u32_e32 v4, s15, v181
	v_add_u32_e32 v6, 0xd00, v180
	v_add_u32_e32 v5, 0x100, v4
	v_cndmask_b32_e64 v5, v6, v5, s[10:11]
	v_cndmask_b32_e64 v3, v5, v4, s[8:9]
	ds_read_b128 v[68:71], v98 offset:0
	ds_read_b128 v[72:75], v98 offset:64
	ds_read_b128 v[76:79], v99 offset:16384
	ds_read_b128 v[80:83], v99 offset:16448
	ds_read_b128 v[84:87], v99 offset:16512
	ds_read_b128 v[88:91], v99 offset:16576
	ds_read2_b32 v[92:93], v0 offset1:16
	ds_read2_b32 v[94:95], v0 offset0:32 offset1:48
	ds_read_b32 v96, v1 offset:0
	ds_read_b128 v[100:103], v2 offset:0
	v_cvt_pk_bf16_f32 v8, v64, v65
	v_cvt_pk_bf16_f32 v9, v66, v67
	v_cvt_pk_bf16_f32 v10, v60, v61
	v_cvt_pk_bf16_f32 v11, v62, v63
	v_cvt_pk_bf16_f32 v12, v52, v53
	v_cvt_pk_bf16_f32 v13, v54, v55
	s_waitcnt lgkmcnt(5)
	v_mfma_f32_16x16x32_bf16 v[140:143], v[68:71], v[8:11], 0
	v_cvt_pk_bf16_f32 v14, v56, v57
	v_cvt_pk_bf16_f32 v15, v58, v59
	v_pk_mul_f32 v[64:65], v[64:65], v[76:77]
	v_pk_mul_f32 v[66:67], v[66:67], v[78:79]
	v_mfma_f32_16x16x32_bf16 v[140:143], v[72:75], v[12:15], v[140:143]
	v_pk_mul_f32 v[60:61], v[60:61], v[80:81]
	v_pk_mul_f32 v[62:63], v[62:63], v[82:83]
	v_pk_mul_f32 v[52:53], v[52:53], v[84:85]
	v_pk_mul_f32 v[54:55], v[54:55], v[86:87]
	s_waitcnt lgkmcnt(4)
	v_pk_mul_f32 v[56:57], v[56:57], v[88:89]
	v_pk_mul_f32 v[58:59], v[58:59], v[90:91]
	ds_read_b128 v[104:107], v98 offset:512
	ds_read_b128 v[108:111], v98 offset:576
	ds_read_b128 v[112:115], v99 offset:16640
	ds_read_b128 v[116:119], v99 offset:16704
	ds_read_b128 v[120:123], v99 offset:16768
	s_waitcnt lgkmcnt(5)
	v_fma_f32 v144, v100, v140, v142
	v_fmac_f32_e32 v144, v101, v96
	v_cndmask_b32_e64 v145, v96, v144, s[10:11]
	v_cndmask_b32_e64 v145, v145, v140, s[8:9]
	v_fma_f32 v50, v102, v140, v143
	v_fmac_f32_e32 v50, v103, v96
	v_mfma_f32_16x16x4_f32 v[64:67], v92, v145, v[64:67]
	v_mfma_f32_16x16x4_f32 v[60:63], v93, v145, v[60:63]
	v_mfma_f32_16x16x4_f32 v[52:55], v94, v145, v[52:55]
	v_mfma_f32_16x16x4_f32 v[56:59], v95, v145, v[56:59]
	v_cndmask_b32_e64 v50, v50, v141, s[8:9]
	ds_write_b32 v3, v50 offset:0
	ds_read_b128 v[128:131], v99 offset:16832
	v_add_u32_e32 v0, 0x400, v0
	ds_read2_b32 v[132:133], v0 offset1:16
	ds_read2_b32 v[134:135], v0 offset0:32 offset1:48
	ds_read_b32 v97, v1 offset:512
	ds_read_b128 v[136:139], v2 offset:16
	v_cvt_pk_bf16_f32 v8, v64, v65
	v_cvt_pk_bf16_f32 v9, v66, v67
	v_cvt_pk_bf16_f32 v10, v60, v61
	v_cvt_pk_bf16_f32 v11, v62, v63
	v_cvt_pk_bf16_f32 v12, v52, v53
	v_cvt_pk_bf16_f32 v13, v54, v55
	s_waitcnt lgkmcnt(5)
	v_mfma_f32_16x16x32_bf16 v[140:143], v[104:107], v[8:11], 0
	v_cvt_pk_bf16_f32 v14, v56, v57
	v_cvt_pk_bf16_f32 v15, v58, v59
	v_pk_mul_f32 v[64:65], v[64:65], v[112:113]
	v_pk_mul_f32 v[66:67], v[66:67], v[114:115]
	v_mfma_f32_16x16x32_bf16 v[140:143], v[108:111], v[12:15], v[140:143]
	v_pk_mul_f32 v[60:61], v[60:61], v[116:117]
	v_pk_mul_f32 v[62:63], v[62:63], v[118:119]
	v_pk_mul_f32 v[52:53], v[52:53], v[120:121]
	v_pk_mul_f32 v[54:55], v[54:55], v[122:123]
	s_waitcnt lgkmcnt(4)
	v_pk_mul_f32 v[56:57], v[56:57], v[128:129]
	v_pk_mul_f32 v[58:59], v[58:59], v[130:131]
	ds_read_b128 v[68:71], v98 offset:1024
	ds_read_b128 v[72:75], v98 offset:1088
	ds_read_b128 v[76:79], v99 offset:16896
	ds_read_b128 v[80:83], v99 offset:16960
	ds_read_b128 v[84:87], v99 offset:17024
	s_waitcnt lgkmcnt(5)
	v_fma_f32 v144, v136, v140, v142
	v_fmac_f32_e32 v144, v137, v97
	v_cndmask_b32_e64 v145, v97, v144, s[10:11]
	v_cndmask_b32_e64 v145, v145, v140, s[8:9]
	v_fma_f32 v50, v138, v140, v143
	v_fmac_f32_e32 v50, v139, v97
	v_mfma_f32_16x16x4_f32 v[64:67], v132, v145, v[64:67]
	v_mfma_f32_16x16x4_f32 v[60:63], v133, v145, v[60:63]
	v_mfma_f32_16x16x4_f32 v[52:55], v134, v145, v[52:55]
	v_mfma_f32_16x16x4_f32 v[56:59], v135, v145, v[56:59]
	v_cndmask_b32_e64 v50, v50, v141, s[8:9]
	ds_write_b32 v3, v50 offset:512
	ds_read_b128 v[88:91], v99 offset:17088
	v_add_u32_e32 v0, 0x400, v0
	ds_read2_b32 v[92:93], v0 offset1:16
	ds_read2_b32 v[94:95], v0 offset0:32 offset1:48
	ds_read_b32 v96, v1 offset:1024
	ds_read_b128 v[100:103], v2 offset:32
	v_cvt_pk_bf16_f32 v8, v64, v65
	v_cvt_pk_bf16_f32 v9, v66, v67
	v_cvt_pk_bf16_f32 v10, v60, v61
	v_cvt_pk_bf16_f32 v11, v62, v63
	v_cvt_pk_bf16_f32 v12, v52, v53
	v_cvt_pk_bf16_f32 v13, v54, v55
	s_waitcnt lgkmcnt(5)
	v_mfma_f32_16x16x32_bf16 v[140:143], v[68:71], v[8:11], 0
	v_cvt_pk_bf16_f32 v14, v56, v57
	v_cvt_pk_bf16_f32 v15, v58, v59
	v_pk_mul_f32 v[64:65], v[64:65], v[76:77]
	v_pk_mul_f32 v[66:67], v[66:67], v[78:79]
	v_mfma_f32_16x16x32_bf16 v[140:143], v[72:75], v[12:15], v[140:143]
	v_pk_mul_f32 v[60:61], v[60:61], v[80:81]
	v_pk_mul_f32 v[62:63], v[62:63], v[82:83]
	v_pk_mul_f32 v[52:53], v[52:53], v[84:85]
	v_pk_mul_f32 v[54:55], v[54:55], v[86:87]
	s_waitcnt lgkmcnt(4)
	v_pk_mul_f32 v[56:57], v[56:57], v[88:89]
	v_pk_mul_f32 v[58:59], v[58:59], v[90:91]
	ds_read_b128 v[104:107], v98 offset:1536
	ds_read_b128 v[108:111], v98 offset:1600
	ds_read_b128 v[112:115], v99 offset:17152
	ds_read_b128 v[116:119], v99 offset:17216
	ds_read_b128 v[120:123], v99 offset:17280
	s_waitcnt lgkmcnt(5)
; __device__ __forceinline__ void scan_head(const Params& p, LAS unsigned char* lds, int bh, const int wave) {
;     ...
;             bf16x8 Pa0, Pa1, Qa0, Qa1; f32x4 Pw0, Pw1, Pw2, Pw3, Qw0, Qw1, Qw2, Qw3, Pcs, Qcs; float Pb0, Pb1, Pb2, Pb3, Pvt, Pvu, Qb0, Qb1, Qb2, Qb3, Qvt, Qvu;
;             SCAN_LD(P, 0);
; #pragma unroll 1
;             for (int pi = 0; pi < 16; pi += 2) {
;                 SCAN_LD(Q, pi + 1);
;                 SCAN_STEP(P, pi);
;                 if (pi + 2 < 16) SCAN_LD(P, pi + 2);
;                 SCAN_STEP(Q, pi + 1);
	v_fma_f32 v144, v100, v140, v142
	v_fmac_f32_e32 v144, v101, v96
	v_cndmask_b32_e64 v145, v96, v144, s[10:11]
	v_cndmask_b32_e64 v145, v145, v140, s[8:9]
	v_fma_f32 v50, v102, v140, v143
	v_fmac_f32_e32 v50, v103, v96
	v_mfma_f32_16x16x4_f32 v[64:67], v92, v145, v[64:67]
	v_mfma_f32_16x16x4_f32 v[60:63], v93, v145, v[60:63]
	v_mfma_f32_16x16x4_f32 v[52:55], v94, v145, v[52:55]
	v_mfma_f32_16x16x4_f32 v[56:59], v95, v145, v[56:59]
	v_cndmask_b32_e64 v50, v50, v141, s[8:9]
	ds_write_b32 v3, v50 offset:1024
	ds_read_b128 v[128:131], v99 offset:17344
	v_add_u32_e32 v0, 0x400, v0
	ds_read2_b32 v[132:133], v0 offset1:16
	ds_read2_b32 v[134:135], v0 offset0:32 offset1:48
	ds_read_b32 v97, v1 offset:1536
	ds_read_b128 v[136:139], v2 offset:48
	v_cvt_pk_bf16_f32 v8, v64, v65
	v_cvt_pk_bf16_f32 v9, v66, v67
	v_cvt_pk_bf16_f32 v10, v60, v61
	v_cvt_pk_bf16_f32 v11, v62, v63
	v_cvt_pk_bf16_f32 v12, v52, v53
	v_cvt_pk_bf16_f32 v13, v54, v55
	s_waitcnt lgkmcnt(5)
	v_mfma_f32_16x16x32_bf16 v[140:143], v[104:107], v[8:11], 0
	v_cvt_pk_bf16_f32 v14, v56, v57
	v_cvt_pk_bf16_f32 v15, v58, v59
	v_pk_mul_f32 v[64:65], v[64:65], v[112:113]
	v_pk_mul_f32 v[66:67], v[66:67], v[114:115]
	v_mfma_f32_16x16x32_bf16 v[140:143], v[108:111], v[12:15], v[140:143]
	v_pk_mul_f32 v[60:61], v[60:61], v[116:117]
	v_pk_mul_f32 v[62:63], v[62:63], v[118:119]
	v_pk_mul_f32 v[52:53], v[52:53], v[120:121]
	v_pk_mul_f32 v[54:55], v[54:55], v[122:123]
	s_waitcnt lgkmcnt(4)
	v_pk_mul_f32 v[56:57], v[56:57], v[128:129]
	v_pk_mul_f32 v[58:59], v[58:59], v[130:131]
	ds_read_b128 v[68:71], v98 offset:2048
	ds_read_b128 v[72:75], v98 offset:2112
	ds_read_b128 v[76:79], v99 offset:17408
	ds_read_b128 v[80:83], v99 offset:17472
	ds_read_b128 v[84:87], v99 offset:17536
	s_waitcnt lgkmcnt(5)
	v_fma_f32 v144, v136, v140, v142
	v_fmac_f32_e32 v144, v137, v97
	v_cndmask_b32_e64 v145, v97, v144, s[10:11]
	v_cndmask_b32_e64 v145, v145, v140, s[8:9]
	v_fma_f32 v50, v138, v140, v143
	v_fmac_f32_e32 v50, v139, v97
	v_mfma_f32_16x16x4_f32 v[64:67], v132, v145, v[64:67]
	v_mfma_f32_16x16x4_f32 v[60:63], v133, v145, v[60:63]
	v_mfma_f32_16x16x4_f32 v[52:55], v134, v145, v[52:55]
	v_mfma_f32_16x16x4_f32 v[56:59], v135, v145, v[56:59]
	v_cndmask_b32_e64 v50, v50, v141, s[8:9]
	ds_write_b32 v3, v50 offset:1536
	ds_read_b128 v[88:91], v99 offset:17600
	v_add_u32_e32 v0, 0x400, v0
	ds_read2_b32 v[92:93], v0 offset1:16
	ds_read2_b32 v[94:95], v0 offset0:32 offset1:48
	ds_read_b32 v96, v1 offset:2048
	ds_read_b128 v[100:103], v2 offset:64
	v_cvt_pk_bf16_f32 v8, v64, v65
	v_cvt_pk_bf16_f32 v9, v66, v67
	v_cvt_pk_bf16_f32 v10, v60, v61
	v_cvt_pk_bf16_f32 v11, v62, v63
	v_cvt_pk_bf16_f32 v12, v52, v53
	v_cvt_pk_bf16_f32 v13, v54, v55
	s_waitcnt lgkmcnt(5)
	v_mfma_f32_16x16x32_bf16 v[140:143], v[68:71], v[8:11], 0
	v_cvt_pk_bf16_f32 v14, v56, v57
	v_cvt_pk_bf16_f32 v15, v58, v59
	v_pk_mul_f32 v[64:65], v[64:65], v[76:77]
	v_pk_mul_f32 v[66:67], v[66:67], v[78:79]
	v_mfma_f32_16x16x32_bf16 v[140:143], v[72:75], v[12:15], v[140:143]
	v_pk_mul_f32 v[60:61], v[60:61], v[80:81]
	v_pk_mul_f32 v[62:63], v[62:63], v[82:83]
	v_pk_mul_f32 v[52:53], v[52:53], v[84:85]
	v_pk_mul_f32 v[54:55], v[54:55], v[86:87]
	s_waitcnt lgkmcnt(4)
	v_pk_mul_f32 v[56:57], v[56:57], v[88:89]
	v_pk_mul_f32 v[58:59], v[58:59], v[90:91]
	ds_read_b128 v[104:107], v98 offset:2560
	ds_read_b128 v[108:111], v98 offset:2624
	ds_read_b128 v[112:115], v99 offset:17664
	ds_read_b128 v[116:119], v99 offset:17728
	ds_read_b128 v[120:123], v99 offset:17792
	s_waitcnt lgkmcnt(5)
	v_fma_f32 v144, v100, v140, v142
	v_fmac_f32_e32 v144, v101, v96
	v_cndmask_b32_e64 v145, v96, v144, s[10:11]
	v_cndmask_b32_e64 v145, v145, v140, s[8:9]
	v_fma_f32 v50, v102, v140, v143
	v_fmac_f32_e32 v50, v103, v96
	v_mfma_f32_16x16x4_f32 v[64:67], v92, v145, v[64:67]
	v_mfma_f32_16x16x4_f32 v[60:63], v93, v145, v[60:63]
	v_mfma_f32_16x16x4_f32 v[52:55], v94, v145, v[52:55]
	v_mfma_f32_16x16x4_f32 v[56:59], v95, v145, v[56:59]
	v_cndmask_b32_e64 v50, v50, v141, s[8:9]
	ds_write_b32 v3, v50 offset:2048
	ds_read_b128 v[128:131], v99 offset:17856
	v_add_u32_e32 v0, 0x400, v0
	ds_read2_b32 v[132:133], v0 offset1:16
	ds_read2_b32 v[134:135], v0 offset0:32 offset1:48
	ds_read_b32 v97, v1 offset:2560
	ds_read_b128 v[136:139], v2 offset:80
	v_cvt_pk_bf16_f32 v8, v64, v65
	v_cvt_pk_bf16_f32 v9, v66, v67
	v_cvt_pk_bf16_f32 v10, v60, v61
	v_cvt_pk_bf16_f32 v11, v62, v63
	v_cvt_pk_bf16_f32 v12, v52, v53
	v_cvt_pk_bf16_f32 v13, v54, v55
	s_waitcnt lgkmcnt(5)
	v_mfma_f32_16x16x32_bf16 v[140:143], v[104:107], v[8:11], 0
	v_cvt_pk_bf16_f32 v14, v56, v57
	v_cvt_pk_bf16_f32 v15, v58, v59
	v_pk_mul_f32 v[64:65], v[64:65], v[112:113]
	v_pk_mul_f32 v[66:67], v[66:67], v[114:115]
	v_mfma_f32_16x16x32_bf16 v[140:143], v[108:111], v[12:15], v[140:143]
	v_pk_mul_f32 v[60:61], v[60:61], v[116:117]
	v_pk_mul_f32 v[62:63], v[62:63], v[118:119]
	v_pk_mul_f32 v[52:53], v[52:53], v[120:121]
	v_pk_mul_f32 v[54:55], v[54:55], v[122:123]
	s_waitcnt lgkmcnt(4)
	v_pk_mul_f32 v[56:57], v[56:57], v[128:129]
	v_pk_mul_f32 v[58:59], v[58:59], v[130:131]
	ds_read_b128 v[68:71], v98 offset:3072
	ds_read_b128 v[72:75], v98 offset:3136
	ds_read_b128 v[76:79], v99 offset:17920
	ds_read_b128 v[80:83], v99 offset:17984
	ds_read_b128 v[84:87], v99 offset:18048
	s_waitcnt lgkmcnt(5)
; __device__ __forceinline__ void scan_head(const Params& p, LAS unsigned char* lds, int bh, const int wave) {
;     ...
;             bf16x8 Pa0, Pa1, Qa0, Qa1; f32x4 Pw0, Pw1, Pw2, Pw3, Qw0, Qw1, Qw2, Qw3, Pcs, Qcs; float Pb0, Pb1, Pb2, Pb3, Pvt, Pvu, Qb0, Qb1, Qb2, Qb3, Qvt, Qvu;
;             SCAN_LD(P, 0);
; #pragma unroll 1
;             for (int pi = 0; pi < 16; pi += 2) {
;                 SCAN_LD(Q, pi + 1);
;                 SCAN_STEP(P, pi);
;                 if (pi + 2 < 16) SCAN_LD(P, pi + 2);
;                 SCAN_STEP(Q, pi + 1);
	v_fma_f32 v144, v136, v140, v142
	v_fmac_f32_e32 v144, v137, v97
	v_cndmask_b32_e64 v145, v97, v144, s[10:11]
	v_cndmask_b32_e64 v145, v145, v140, s[8:9]
	v_fma_f32 v50, v138, v140, v143
	v_fmac_f32_e32 v50, v139, v97
	v_mfma_f32_16x16x4_f32 v[64:67], v132, v145, v[64:67]
	v_mfma_f32_16x16x4_f32 v[60:63], v133, v145, v[60:63]
	v_mfma_f32_16x16x4_f32 v[52:55], v134, v145, v[52:55]
	v_mfma_f32_16x16x4_f32 v[56:59], v135, v145, v[56:59]
	v_cndmask_b32_e64 v50, v50, v141, s[8:9]
	ds_write_b32 v3, v50 offset:2560
	ds_read_b128 v[88:91], v99 offset:18112
	v_add_u32_e32 v0, 0x400, v0
	ds_read2_b32 v[92:93], v0 offset1:16
	ds_read2_b32 v[94:95], v0 offset0:32 offset1:48
	ds_read_b32 v96, v1 offset:3072
	ds_read_b128 v[100:103], v2 offset:96
	v_cvt_pk_bf16_f32 v8, v64, v65
	v_cvt_pk_bf16_f32 v9, v66, v67
	v_cvt_pk_bf16_f32 v10, v60, v61
	v_cvt_pk_bf16_f32 v11, v62, v63
	v_cvt_pk_bf16_f32 v12, v52, v53
	v_cvt_pk_bf16_f32 v13, v54, v55
	s_waitcnt lgkmcnt(5)
	v_mfma_f32_16x16x32_bf16 v[140:143], v[68:71], v[8:11], 0
	v_cvt_pk_bf16_f32 v14, v56, v57
	v_cvt_pk_bf16_f32 v15, v58, v59
	v_pk_mul_f32 v[64:65], v[64:65], v[76:77]
	v_pk_mul_f32 v[66:67], v[66:67], v[78:79]
	v_mfma_f32_16x16x32_bf16 v[140:143], v[72:75], v[12:15], v[140:143]
	v_pk_mul_f32 v[60:61], v[60:61], v[80:81]
	v_pk_mul_f32 v[62:63], v[62:63], v[82:83]
	v_pk_mul_f32 v[52:53], v[52:53], v[84:85]
	v_pk_mul_f32 v[54:55], v[54:55], v[86:87]
	s_waitcnt lgkmcnt(4)
	v_pk_mul_f32 v[56:57], v[56:57], v[88:89]
	v_pk_mul_f32 v[58:59], v[58:59], v[90:91]
	ds_read_b128 v[104:107], v98 offset:3584
	ds_read_b128 v[108:111], v98 offset:3648
	ds_read_b128 v[112:115], v99 offset:18176
	ds_read_b128 v[116:119], v99 offset:18240
	ds_read_b128 v[120:123], v99 offset:18304
	s_waitcnt lgkmcnt(5)
	v_fma_f32 v144, v100, v140, v142
	v_fmac_f32_e32 v144, v101, v96
	v_cndmask_b32_e64 v145, v96, v144, s[10:11]
	v_cndmask_b32_e64 v145, v145, v140, s[8:9]
	v_fma_f32 v50, v102, v140, v143
	v_fmac_f32_e32 v50, v103, v96
	v_mfma_f32_16x16x4_f32 v[64:67], v92, v145, v[64:67]
	v_mfma_f32_16x16x4_f32 v[60:63], v93, v145, v[60:63]
	v_mfma_f32_16x16x4_f32 v[52:55], v94, v145, v[52:55]
	v_mfma_f32_16x16x4_f32 v[56:59], v95, v145, v[56:59]
	v_cndmask_b32_e64 v50, v50, v141, s[8:9]
	ds_write_b32 v3, v50 offset:3072
	ds_read_b128 v[128:131], v99 offset:18368
	v_add_u32_e32 v0, 0x400, v0
	ds_read2_b32 v[132:133], v0 offset1:16
	ds_read2_b32 v[134:135], v0 offset0:32 offset1:48
	ds_read_b32 v97, v1 offset:3584
	ds_read_b128 v[136:139], v2 offset:112
	v_cvt_pk_bf16_f32 v8, v64, v65
	v_cvt_pk_bf16_f32 v9, v66, v67
	v_cvt_pk_bf16_f32 v10, v60, v61
	v_cvt_pk_bf16_f32 v11, v62, v63
	v_cvt_pk_bf16_f32 v12, v52, v53
	v_cvt_pk_bf16_f32 v13, v54, v55
	s_waitcnt lgkmcnt(5)
	v_mfma_f32_16x16x32_bf16 v[140:143], v[104:107], v[8:11], 0
	v_cvt_pk_bf16_f32 v14, v56, v57
	v_cvt_pk_bf16_f32 v15, v58, v59
	v_pk_mul_f32 v[64:65], v[64:65], v[112:113]
	v_pk_mul_f32 v[66:67], v[66:67], v[114:115]
	v_mfma_f32_16x16x32_bf16 v[140:143], v[108:111], v[12:15], v[140:143]
	v_pk_mul_f32 v[60:61], v[60:61], v[116:117]
	v_pk_mul_f32 v[62:63], v[62:63], v[118:119]
	v_pk_mul_f32 v[52:53], v[52:53], v[120:121]
	v_pk_mul_f32 v[54:55], v[54:55], v[122:123]
	s_waitcnt lgkmcnt(4)
	v_pk_mul_f32 v[56:57], v[56:57], v[128:129]
	v_pk_mul_f32 v[58:59], v[58:59], v[130:131]
	ds_read_b128 v[68:71], v98 offset:4096
	ds_read_b128 v[72:75], v98 offset:4160
	ds_read_b128 v[76:79], v99 offset:18432
	ds_read_b128 v[80:83], v99 offset:18496
	ds_read_b128 v[84:87], v99 offset:18560
	s_waitcnt lgkmcnt(5)
	v_fma_f32 v144, v136, v140, v142
	v_fmac_f32_e32 v144, v137, v97
	v_cndmask_b32_e64 v145, v97, v144, s[10:11]
	v_cndmask_b32_e64 v145, v145, v140, s[8:9]
	v_fma_f32 v50, v138, v140, v143
	v_fmac_f32_e32 v50, v139, v97
	v_mfma_f32_16x16x4_f32 v[64:67], v132, v145, v[64:67]
	v_mfma_f32_16x16x4_f32 v[60:63], v133, v145, v[60:63]
	v_mfma_f32_16x16x4_f32 v[52:55], v134, v145, v[52:55]
	v_mfma_f32_16x16x4_f32 v[56:59], v135, v145, v[56:59]
	v_cndmask_b32_e64 v50, v50, v141, s[8:9]
	ds_write_b32 v3, v50 offset:3584
	ds_read_b128 v[88:91], v99 offset:18624
	v_add_u32_e32 v0, 0x400, v0
	ds_read2_b32 v[92:93], v0 offset1:16
	ds_read2_b32 v[94:95], v0 offset0:32 offset1:48
	ds_read_b32 v96, v1 offset:4096
	ds_read_b128 v[100:103], v2 offset:128
	v_cvt_pk_bf16_f32 v8, v64, v65
	v_cvt_pk_bf16_f32 v9, v66, v67
	v_cvt_pk_bf16_f32 v10, v60, v61
	v_cvt_pk_bf16_f32 v11, v62, v63
	v_cvt_pk_bf16_f32 v12, v52, v53
	v_cvt_pk_bf16_f32 v13, v54, v55
	s_waitcnt lgkmcnt(5)
	v_mfma_f32_16x16x32_bf16 v[140:143], v[68:71], v[8:11], 0
	v_cvt_pk_bf16_f32 v14, v56, v57
	v_cvt_pk_bf16_f32 v15, v58, v59
	v_pk_mul_f32 v[64:65], v[64:65], v[76:77]
	v_pk_mul_f32 v[66:67], v[66:67], v[78:79]
	v_mfma_f32_16x16x32_bf16 v[140:143], v[72:75], v[12:15], v[140:143]
	v_pk_mul_f32 v[60:61], v[60:61], v[80:81]
	v_pk_mul_f32 v[62:63], v[62:63], v[82:83]
	v_pk_mul_f32 v[52:53], v[52:53], v[84:85]
	v_pk_mul_f32 v[54:55], v[54:55], v[86:87]
	s_waitcnt lgkmcnt(4)
	v_pk_mul_f32 v[56:57], v[56:57], v[88:89]
	v_pk_mul_f32 v[58:59], v[58:59], v[90:91]
	ds_read_b128 v[104:107], v98 offset:4608
	ds_read_b128 v[108:111], v98 offset:4672
	ds_read_b128 v[112:115], v99 offset:18688
	ds_read_b128 v[116:119], v99 offset:18752
	ds_read_b128 v[120:123], v99 offset:18816
	s_waitcnt lgkmcnt(5)
; __device__ __forceinline__ void scan_head(const Params& p, LAS unsigned char* lds, int bh, const int wave) {
;     ...
;             bf16x8 Pa0, Pa1, Qa0, Qa1; f32x4 Pw0, Pw1, Pw2, Pw3, Qw0, Qw1, Qw2, Qw3, Pcs, Qcs; float Pb0, Pb1, Pb2, Pb3, Pvt, Pvu, Qb0, Qb1, Qb2, Qb3, Qvt, Qvu;
;             SCAN_LD(P, 0);
; #pragma unroll 1
;             for (int pi = 0; pi < 16; pi += 2) {
;                 SCAN_LD(Q, pi + 1);
;                 SCAN_STEP(P, pi);
;                 if (pi + 2 < 16) SCAN_LD(P, pi + 2);
;                 SCAN_STEP(Q, pi + 1);
	v_fma_f32 v144, v100, v140, v142
	v_fmac_f32_e32 v144, v101, v96
	v_cndmask_b32_e64 v145, v96, v144, s[10:11]
	v_cndmask_b32_e64 v145, v145, v140, s[8:9]
	v_fma_f32 v50, v102, v140, v143
	v_fmac_f32_e32 v50, v103, v96
	v_mfma_f32_16x16x4_f32 v[64:67], v92, v145, v[64:67]
	v_mfma_f32_16x16x4_f32 v[60:63], v93, v145, v[60:63]
	v_mfma_f32_16x16x4_f32 v[52:55], v94, v145, v[52:55]
	v_mfma_f32_16x16x4_f32 v[56:59], v95, v145, v[56:59]
	v_cndmask_b32_e64 v50, v50, v141, s[8:9]
	ds_write_b32 v3, v50 offset:4096
	ds_read_b128 v[128:131], v99 offset:18880
	v_add_u32_e32 v0, 0x400, v0
	ds_read2_b32 v[132:133], v0 offset1:16
	ds_read2_b32 v[134:135], v0 offset0:32 offset1:48
	ds_read_b32 v97, v1 offset:4608
	ds_read_b128 v[136:139], v2 offset:144
	v_cvt_pk_bf16_f32 v8, v64, v65
	v_cvt_pk_bf16_f32 v9, v66, v67
	v_cvt_pk_bf16_f32 v10, v60, v61
	v_cvt_pk_bf16_f32 v11, v62, v63
	v_cvt_pk_bf16_f32 v12, v52, v53
	v_cvt_pk_bf16_f32 v13, v54, v55
	s_waitcnt lgkmcnt(5)
	v_mfma_f32_16x16x32_bf16 v[140:143], v[104:107], v[8:11], 0
	v_cvt_pk_bf16_f32 v14, v56, v57
	v_cvt_pk_bf16_f32 v15, v58, v59
	v_pk_mul_f32 v[64:65], v[64:65], v[112:113]
	v_pk_mul_f32 v[66:67], v[66:67], v[114:115]
	v_mfma_f32_16x16x32_bf16 v[140:143], v[108:111], v[12:15], v[140:143]
	v_pk_mul_f32 v[60:61], v[60:61], v[116:117]
	v_pk_mul_f32 v[62:63], v[62:63], v[118:119]
	v_pk_mul_f32 v[52:53], v[52:53], v[120:121]
	v_pk_mul_f32 v[54:55], v[54:55], v[122:123]
	s_waitcnt lgkmcnt(4)
	v_pk_mul_f32 v[56:57], v[56:57], v[128:129]
	v_pk_mul_f32 v[58:59], v[58:59], v[130:131]
	ds_read_b128 v[68:71], v98 offset:5120
	ds_read_b128 v[72:75], v98 offset:5184
	ds_read_b128 v[76:79], v99 offset:18944
	ds_read_b128 v[80:83], v99 offset:19008
	ds_read_b128 v[84:87], v99 offset:19072
	s_waitcnt lgkmcnt(5)
	v_fma_f32 v144, v136, v140, v142
	v_fmac_f32_e32 v144, v137, v97
	v_cndmask_b32_e64 v145, v97, v144, s[10:11]
	v_cndmask_b32_e64 v145, v145, v140, s[8:9]
	v_fma_f32 v50, v138, v140, v143
	v_fmac_f32_e32 v50, v139, v97
	v_mfma_f32_16x16x4_f32 v[64:67], v132, v145, v[64:67]
	v_mfma_f32_16x16x4_f32 v[60:63], v133, v145, v[60:63]
	v_mfma_f32_16x16x4_f32 v[52:55], v134, v145, v[52:55]
	v_mfma_f32_16x16x4_f32 v[56:59], v135, v145, v[56:59]
	v_cndmask_b32_e64 v50, v50, v141, s[8:9]
	ds_write_b32 v3, v50 offset:4608
	ds_read_b128 v[88:91], v99 offset:19136
	v_add_u32_e32 v0, 0x400, v0
	ds_read2_b32 v[92:93], v0 offset1:16
	ds_read2_b32 v[94:95], v0 offset0:32 offset1:48
	ds_read_b32 v96, v1 offset:5120
	ds_read_b128 v[100:103], v2 offset:160
	v_cvt_pk_bf16_f32 v8, v64, v65
	v_cvt_pk_bf16_f32 v9, v66, v67
	v_cvt_pk_bf16_f32 v10, v60, v61
	v_cvt_pk_bf16_f32 v11, v62, v63
	v_cvt_pk_bf16_f32 v12, v52, v53
	v_cvt_pk_bf16_f32 v13, v54, v55
	s_waitcnt lgkmcnt(5)
	v_mfma_f32_16x16x32_bf16 v[140:143], v[68:71], v[8:11], 0
	v_cvt_pk_bf16_f32 v14, v56, v57
	v_cvt_pk_bf16_f32 v15, v58, v59
	v_pk_mul_f32 v[64:65], v[64:65], v[76:77]
	v_pk_mul_f32 v[66:67], v[66:67], v[78:79]
	v_mfma_f32_16x16x32_bf16 v[140:143], v[72:75], v[12:15], v[140:143]
	v_pk_mul_f32 v[60:61], v[60:61], v[80:81]
	v_pk_mul_f32 v[62:63], v[62:63], v[82:83]
	v_pk_mul_f32 v[52:53], v[52:53], v[84:85]
	v_pk_mul_f32 v[54:55], v[54:55], v[86:87]
	s_waitcnt lgkmcnt(4)
	v_pk_mul_f32 v[56:57], v[56:57], v[88:89]
	v_pk_mul_f32 v[58:59], v[58:59], v[90:91]
	ds_read_b128 v[104:107], v98 offset:5632
	ds_read_b128 v[108:111], v98 offset:5696
	ds_read_b128 v[112:115], v99 offset:19200
	ds_read_b128 v[116:119], v99 offset:19264
	ds_read_b128 v[120:123], v99 offset:19328
	s_waitcnt lgkmcnt(5)
	v_fma_f32 v144, v100, v140, v142
	v_fmac_f32_e32 v144, v101, v96
	v_cndmask_b32_e64 v145, v96, v144, s[10:11]
	v_cndmask_b32_e64 v145, v145, v140, s[8:9]
	v_fma_f32 v50, v102, v140, v143
	v_fmac_f32_e32 v50, v103, v96
	v_mfma_f32_16x16x4_f32 v[64:67], v92, v145, v[64:67]
	v_mfma_f32_16x16x4_f32 v[60:63], v93, v145, v[60:63]
	v_mfma_f32_16x16x4_f32 v[52:55], v94, v145, v[52:55]
	v_mfma_f32_16x16x4_f32 v[56:59], v95, v145, v[56:59]
	v_cndmask_b32_e64 v50, v50, v141, s[8:9]
	ds_write_b32 v3, v50 offset:5120
	ds_read_b128 v[128:131], v99 offset:19392
	v_add_u32_e32 v0, 0x400, v0
	ds_read2_b32 v[132:133], v0 offset1:16
	ds_read2_b32 v[134:135], v0 offset0:32 offset1:48
	ds_read_b32 v97, v1 offset:5632
	ds_read_b128 v[136:139], v2 offset:176
	v_cvt_pk_bf16_f32 v8, v64, v65
	v_cvt_pk_bf16_f32 v9, v66, v67
	v_cvt_pk_bf16_f32 v10, v60, v61
	v_cvt_pk_bf16_f32 v11, v62, v63
	v_cvt_pk_bf16_f32 v12, v52, v53
	v_cvt_pk_bf16_f32 v13, v54, v55
	s_waitcnt lgkmcnt(5)
	v_mfma_f32_16x16x32_bf16 v[140:143], v[104:107], v[8:11], 0
	v_cvt_pk_bf16_f32 v14, v56, v57
	v_cvt_pk_bf16_f32 v15, v58, v59
	v_pk_mul_f32 v[64:65], v[64:65], v[112:113]
	v_pk_mul_f32 v[66:67], v[66:67], v[114:115]
	v_mfma_f32_16x16x32_bf16 v[140:143], v[108:111], v[12:15], v[140:143]
	v_pk_mul_f32 v[60:61], v[60:61], v[116:117]
	v_pk_mul_f32 v[62:63], v[62:63], v[118:119]
	v_pk_mul_f32 v[52:53], v[52:53], v[120:121]
	v_pk_mul_f32 v[54:55], v[54:55], v[122:123]
	s_waitcnt lgkmcnt(4)
	v_pk_mul_f32 v[56:57], v[56:57], v[128:129]
	v_pk_mul_f32 v[58:59], v[58:59], v[130:131]
	ds_read_b128 v[68:71], v98 offset:6144
	ds_read_b128 v[72:75], v98 offset:6208
	ds_read_b128 v[76:79], v99 offset:19456
	ds_read_b128 v[80:83], v99 offset:19520
	ds_read_b128 v[84:87], v99 offset:19584
	s_waitcnt lgkmcnt(5)
; __device__ __forceinline__ void scan_head(const Params& p, LAS unsigned char* lds, int bh, const int wave) {
;     ...
;             bf16x8 Pa0, Pa1, Qa0, Qa1; f32x4 Pw0, Pw1, Pw2, Pw3, Qw0, Qw1, Qw2, Qw3, Pcs, Qcs; float Pb0, Pb1, Pb2, Pb3, Pvt, Pvu, Qb0, Qb1, Qb2, Qb3, Qvt, Qvu;
;             SCAN_LD(P, 0);
; #pragma unroll 1
;             for (int pi = 0; pi < 16; pi += 2) {
;                 SCAN_LD(Q, pi + 1);
;                 SCAN_STEP(P, pi);
;                 if (pi + 2 < 16) SCAN_LD(P, pi + 2);
;                 SCAN_STEP(Q, pi + 1);
	v_fma_f32 v144, v136, v140, v142
	v_fmac_f32_e32 v144, v137, v97
	v_cndmask_b32_e64 v145, v97, v144, s[10:11]
	v_cndmask_b32_e64 v145, v145, v140, s[8:9]
	v_fma_f32 v50, v138, v140, v143
	v_fmac_f32_e32 v50, v139, v97
	v_mfma_f32_16x16x4_f32 v[64:67], v132, v145, v[64:67]
	v_mfma_f32_16x16x4_f32 v[60:63], v133, v145, v[60:63]
	v_mfma_f32_16x16x4_f32 v[52:55], v134, v145, v[52:55]
	v_mfma_f32_16x16x4_f32 v[56:59], v135, v145, v[56:59]
	v_cndmask_b32_e64 v50, v50, v141, s[8:9]
	ds_write_b32 v3, v50 offset:5632
	ds_read_b128 v[88:91], v99 offset:19648
	v_add_u32_e32 v0, 0x400, v0
	ds_read2_b32 v[92:93], v0 offset1:16
	ds_read2_b32 v[94:95], v0 offset0:32 offset1:48
	ds_read_b32 v96, v1 offset:6144
	ds_read_b128 v[100:103], v2 offset:192
	v_cvt_pk_bf16_f32 v8, v64, v65
	v_cvt_pk_bf16_f32 v9, v66, v67
	v_cvt_pk_bf16_f32 v10, v60, v61
	v_cvt_pk_bf16_f32 v11, v62, v63
	v_cvt_pk_bf16_f32 v12, v52, v53
	v_cvt_pk_bf16_f32 v13, v54, v55
	s_waitcnt lgkmcnt(5)
	v_mfma_f32_16x16x32_bf16 v[140:143], v[68:71], v[8:11], 0
	v_cvt_pk_bf16_f32 v14, v56, v57
	v_cvt_pk_bf16_f32 v15, v58, v59
	v_pk_mul_f32 v[64:65], v[64:65], v[76:77]
	v_pk_mul_f32 v[66:67], v[66:67], v[78:79]
	v_mfma_f32_16x16x32_bf16 v[140:143], v[72:75], v[12:15], v[140:143]
	v_pk_mul_f32 v[60:61], v[60:61], v[80:81]
	v_pk_mul_f32 v[62:63], v[62:63], v[82:83]
	v_pk_mul_f32 v[52:53], v[52:53], v[84:85]
	v_pk_mul_f32 v[54:55], v[54:55], v[86:87]
	s_waitcnt lgkmcnt(4)
	v_pk_mul_f32 v[56:57], v[56:57], v[88:89]
	v_pk_mul_f32 v[58:59], v[58:59], v[90:91]
	ds_read_b128 v[104:107], v98 offset:6656
	ds_read_b128 v[108:111], v98 offset:6720
	ds_read_b128 v[112:115], v99 offset:19712
	ds_read_b128 v[116:119], v99 offset:19776
	ds_read_b128 v[120:123], v99 offset:19840
	s_waitcnt lgkmcnt(5)
	v_fma_f32 v144, v100, v140, v142
	v_fmac_f32_e32 v144, v101, v96
	v_cndmask_b32_e64 v145, v96, v144, s[10:11]
	v_cndmask_b32_e64 v145, v145, v140, s[8:9]
	v_fma_f32 v50, v102, v140, v143
	v_fmac_f32_e32 v50, v103, v96
	v_mfma_f32_16x16x4_f32 v[64:67], v92, v145, v[64:67]
	v_mfma_f32_16x16x4_f32 v[60:63], v93, v145, v[60:63]
	v_mfma_f32_16x16x4_f32 v[52:55], v94, v145, v[52:55]
	v_mfma_f32_16x16x4_f32 v[56:59], v95, v145, v[56:59]
	v_cndmask_b32_e64 v50, v50, v141, s[8:9]
	ds_write_b32 v3, v50 offset:6144
	ds_read_b128 v[128:131], v99 offset:19904
	v_add_u32_e32 v0, 0x400, v0
	ds_read2_b32 v[132:133], v0 offset1:16
	ds_read2_b32 v[134:135], v0 offset0:32 offset1:48
	ds_read_b32 v97, v1 offset:6656
	ds_read_b128 v[136:139], v2 offset:208
	v_cvt_pk_bf16_f32 v8, v64, v65
	v_cvt_pk_bf16_f32 v9, v66, v67
	v_cvt_pk_bf16_f32 v10, v60, v61
	v_cvt_pk_bf16_f32 v11, v62, v63
	v_cvt_pk_bf16_f32 v12, v52, v53
	v_cvt_pk_bf16_f32 v13, v54, v55
	s_waitcnt lgkmcnt(5)
	v_mfma_f32_16x16x32_bf16 v[140:143], v[104:107], v[8:11], 0
	v_cvt_pk_bf16_f32 v14, v56, v57
	v_cvt_pk_bf16_f32 v15, v58, v59
	v_pk_mul_f32 v[64:65], v[64:65], v[112:113]
	v_pk_mul_f32 v[66:67], v[66:67], v[114:115]
	v_mfma_f32_16x16x32_bf16 v[140:143], v[108:111], v[12:15], v[140:143]
	v_pk_mul_f32 v[60:61], v[60:61], v[116:117]
	v_pk_mul_f32 v[62:63], v[62:63], v[118:119]
	v_pk_mul_f32 v[52:53], v[52:53], v[120:121]
	v_pk_mul_f32 v[54:55], v[54:55], v[122:123]
	s_waitcnt lgkmcnt(4)
	v_pk_mul_f32 v[56:57], v[56:57], v[128:129]
	v_pk_mul_f32 v[58:59], v[58:59], v[130:131]
	ds_read_b128 v[68:71], v98 offset:7168
	ds_read_b128 v[72:75], v98 offset:7232
	ds_read_b128 v[76:79], v99 offset:19968
	ds_read_b128 v[80:83], v99 offset:20032
	ds_read_b128 v[84:87], v99 offset:20096
	s_waitcnt lgkmcnt(5)
; __device__ __forceinline__ void scan_head(const Params& p, LAS unsigned char* lds, int bh, const int wave) {
;     ...
;             bf16x8 Pa0, Pa1, Qa0, Qa1; f32x4 Pw0, Pw1, Pw2, Pw3, Qw0, Qw1, Qw2, Qw3, Pcs, Qcs; float Pb0, Pb1, Pb2, Pb3, Pvt, Pvu, Qb0, Qb1, Qb2, Qb3, Qvt, Qvu;
;             SCAN_LD(P, 0);
; #pragma unroll 1
;             for (int pi = 0; pi < 16; pi += 2) {
;                 SCAN_LD(Q, pi + 1);
;                 SCAN_STEP(P, pi);
;                 if (pi + 2 < 16) SCAN_LD(P, pi + 2);
;                 SCAN_STEP(Q, pi + 1);
;             }
	v_fma_f32 v144, v136, v140, v142
	v_fmac_f32_e32 v144, v137, v97
	v_cndmask_b32_e64 v145, v97, v144, s[10:11]
	v_cndmask_b32_e64 v145, v145, v140, s[8:9]
	v_fma_f32 v50, v138, v140, v143
	v_fmac_f32_e32 v50, v139, v97
	v_mfma_f32_16x16x4_f32 v[64:67], v132, v145, v[64:67]
	v_mfma_f32_16x16x4_f32 v[60:63], v133, v145, v[60:63]
	v_mfma_f32_16x16x4_f32 v[52:55], v134, v145, v[52:55]
	v_mfma_f32_16x16x4_f32 v[56:59], v135, v145, v[56:59]
	v_cndmask_b32_e64 v50, v50, v141, s[8:9]
	ds_write_b32 v3, v50 offset:6656
	ds_read_b128 v[88:91], v99 offset:20160
	v_add_u32_e32 v0, 0x400, v0
	ds_read2_b32 v[92:93], v0 offset1:16
	ds_read2_b32 v[94:95], v0 offset0:32 offset1:48
	ds_read_b32 v96, v1 offset:7168
	ds_read_b128 v[100:103], v2 offset:224
	v_cvt_pk_bf16_f32 v8, v64, v65
	v_cvt_pk_bf16_f32 v9, v66, v67
	v_cvt_pk_bf16_f32 v10, v60, v61
	v_cvt_pk_bf16_f32 v11, v62, v63
	v_cvt_pk_bf16_f32 v12, v52, v53
	v_cvt_pk_bf16_f32 v13, v54, v55
	s_waitcnt lgkmcnt(5)
	v_mfma_f32_16x16x32_bf16 v[140:143], v[68:71], v[8:11], 0
	v_cvt_pk_bf16_f32 v14, v56, v57
	v_cvt_pk_bf16_f32 v15, v58, v59
	v_pk_mul_f32 v[64:65], v[64:65], v[76:77]
	v_pk_mul_f32 v[66:67], v[66:67], v[78:79]
	v_mfma_f32_16x16x32_bf16 v[140:143], v[72:75], v[12:15], v[140:143]
	v_pk_mul_f32 v[60:61], v[60:61], v[80:81]
	v_pk_mul_f32 v[62:63], v[62:63], v[82:83]
	v_pk_mul_f32 v[52:53], v[52:53], v[84:85]
	v_pk_mul_f32 v[54:55], v[54:55], v[86:87]
	s_waitcnt lgkmcnt(4)
	v_pk_mul_f32 v[56:57], v[56:57], v[88:89]
	v_pk_mul_f32 v[58:59], v[58:59], v[90:91]
	ds_read_b128 v[104:107], v98 offset:7680
	ds_read_b128 v[108:111], v98 offset:7744
	ds_read_b128 v[112:115], v99 offset:20224
	ds_read_b128 v[116:119], v99 offset:20288
	ds_read_b128 v[120:123], v99 offset:20352
	s_waitcnt lgkmcnt(5)
	v_fma_f32 v144, v100, v140, v142
	v_fmac_f32_e32 v144, v101, v96
	v_cndmask_b32_e64 v145, v96, v144, s[10:11]
	v_cndmask_b32_e64 v145, v145, v140, s[8:9]
	v_fma_f32 v50, v102, v140, v143
	v_fmac_f32_e32 v50, v103, v96
	v_mfma_f32_16x16x4_f32 v[64:67], v92, v145, v[64:67]
	v_mfma_f32_16x16x4_f32 v[60:63], v93, v145, v[60:63]
	v_mfma_f32_16x16x4_f32 v[52:55], v94, v145, v[52:55]
	v_mfma_f32_16x16x4_f32 v[56:59], v95, v145, v[56:59]
	v_cndmask_b32_e64 v50, v50, v141, s[8:9]
	ds_write_b32 v3, v50 offset:7168
	ds_read_b128 v[128:131], v99 offset:20416
	v_add_u32_e32 v0, 0x400, v0
	ds_read2_b32 v[132:133], v0 offset1:16
	ds_read2_b32 v[134:135], v0 offset0:32 offset1:48
	ds_read_b32 v97, v1 offset:7680
	ds_read_b128 v[136:139], v2 offset:240
	v_cvt_pk_bf16_f32 v8, v64, v65
	v_cvt_pk_bf16_f32 v9, v66, v67
	v_cvt_pk_bf16_f32 v10, v60, v61
	v_cvt_pk_bf16_f32 v11, v62, v63
	v_cvt_pk_bf16_f32 v12, v52, v53
	v_cvt_pk_bf16_f32 v13, v54, v55
	s_waitcnt lgkmcnt(5)
	v_mfma_f32_16x16x32_bf16 v[140:143], v[104:107], v[8:11], 0
	v_cvt_pk_bf16_f32 v14, v56, v57
	v_cvt_pk_bf16_f32 v15, v58, v59
	v_pk_mul_f32 v[64:65], v[64:65], v[112:113]
	v_pk_mul_f32 v[66:67], v[66:67], v[114:115]
	v_mfma_f32_16x16x32_bf16 v[140:143], v[108:111], v[12:15], v[140:143]
	v_pk_mul_f32 v[60:61], v[60:61], v[116:117]
	v_pk_mul_f32 v[62:63], v[62:63], v[118:119]
	v_pk_mul_f32 v[52:53], v[52:53], v[120:121]
	v_pk_mul_f32 v[54:55], v[54:55], v[122:123]
	s_waitcnt lgkmcnt(4)
	v_pk_mul_f32 v[56:57], v[56:57], v[128:129]
	v_pk_mul_f32 v[58:59], v[58:59], v[130:131]
	s_waitcnt lgkmcnt(0)
	s_nop 1
	v_fma_f32 v144, v136, v140, v142
	v_fmac_f32_e32 v144, v137, v97
	v_cndmask_b32_e64 v145, v97, v144, s[10:11]
	v_cndmask_b32_e64 v145, v145, v140, s[8:9]
	v_fma_f32 v50, v138, v140, v143
	v_fmac_f32_e32 v50, v139, v97
	v_mfma_f32_16x16x4_f32 v[64:67], v132, v145, v[64:67]
	v_mfma_f32_16x16x4_f32 v[60:63], v133, v145, v[60:63]
	v_mfma_f32_16x16x4_f32 v[52:55], v134, v145, v[52:55]
	v_mfma_f32_16x16x4_f32 v[56:59], v135, v145, v[56:59]
	v_cndmask_b32_e64 v50, v50, v141, s[8:9]
	ds_write_b32 v3, v50 offset:7680
	s_nop 7

; #define LAS __attribute__((address_space(3)))
; __device__ __forceinline__ void cvt_item_lds(const float* src, int ld_src, fp8_t* dst, int ld_dst, LAS unsigned char* lds, int tid, int wv) {
;     const int lane = tid & 63;
;     const float* s = src + (size_t)(16 * wv) * ld_src + 4 * lane;
;     f32x4 va[16], vb[16];
;     cvt8_load(va, s, ld_src);
; #pragma unroll
;     for (int t = 0; t < 8; t += 2) {
;         cvt8_load(vb, s + (t + 1) * 256, ld_src); __builtin_amdgcn_sched_barrier(0);
; __device__ __forceinline__ void conv_queue(const Params& p, LAS unsigned char* lds, const int wave, const int cw, const int first, const int last, const int slot_off = LDS_MISC) {
;     ...
;     for (;;) {
;         __syncthreads();
;         if (tid == 0) *slot = first + (int)atomicAdd(&p.ctl[cw], 1u);
;         __syncthreads();
;         const int it = *slot;
;         if (it >= last) break;
;         if (it < N_GU) { const int e = it >> 5, rem = it & 31, kb = rem >> 1, nh = rem & 1;
;             const float* src = p.w_gu + (size_t)e * ND * (2 * DFF) + (size_t)(kb * 128) * (2 * DFF) + nh * 2048;
;             fp8_t* dst = p.wt_gu + (size_t)e * (2 * DFF) * ND + (size_t)(nh * 2048) * ND + kb * 128;
;             cvt_item_lds(src, 2 * DFF, dst, ND, lds, tid, wave); }
;         else { const int j = it - N_GU, e = j >> 4, kb = j & 15;
;             const float* src = p.w_down + (size_t)e * DFF * ND + (size_t)(kb * 128) * ND;
;             fp8_t* dst = p.wt_down + (size_t)e * ND * DFF + kb * 128;
;             cvt_item_lds(src, ND, dst, DFF, lds, tid, wave); }
.LBB0_822:
	s_or_b64 exec, exec, s[48:49]
	s_waitcnt lgkmcnt(0)
	s_barrier
	ds_read_b32 v0, v209
	s_movk_i32 s2, 0x45f
	s_mov_b64 s[48:49], -1
	s_waitcnt lgkmcnt(0)
	v_cmp_lt_i32_e32 vcc, s2, v0
	v_readfirstlane_b32 s33, v0
	s_cbranch_vccnz .LBB0_817
	s_cmpk_gt_i32 s33, 0x3ff
	s_cbranch_scc0 .LBB0_825
	s_add_i32 s2, s33, 0xfffffc00
	s_lshr_b32 s4, s2, 4
	v_readlane_b32 s16, v254, 22
	s_lshl_b64 s[34:35], s[4:5], 22
	s_lshl_b64 s[48:49], s[4:5], 24
	v_readlane_b32 s20, v254, 26
	v_readlane_b32 s21, v254, 27
	s_add_u32 s2, s20, s48
	s_addc_u32 s4, s21, s49
	s_lshl_b32 s48, s33, 7
	s_and_b32 s48, s48, 0x780
	s_lshl_b32 s49, s48, 13
	s_add_u32 s2, s2, s49
	s_addc_u32 s4, s4, 0
	s_add_u32 s34, s56, s34
	s_addc_u32 s35, s57, s35
	s_add_u32 s50, s34, s48
	s_addc_u32 s51, s35, 0
	s_add_u32 s48, s2, s14
	s_addc_u32 s49, s4, s15
	v_lshl_add_u64 v[172:173], s[48:49], 0, v[128:129]
	s_movk_i32 s2, 0x2000
	v_add_co_u32_e32 v174, vcc, s2, v172
	s_movk_i32 s2, 0x3000
	s_nop 0
	v_addc_co_u32_e32 v175, vcc, 0, v173, vcc
	v_add_co_u32_e32 v142, vcc, s2, v172
	s_movk_i32 s2, 0x6000
	s_nop 0
	v_addc_co_u32_e32 v143, vcc, 0, v173, vcc
	v_add_co_u32_e32 v176, vcc, s13, v172
	v_readlane_b32 s17, v254, 23
	s_nop 0
	v_addc_co_u32_e32 v177, vcc, 0, v173, vcc
	v_add_co_u32_e32 v144, vcc, s67, v172
	v_readlane_b32 s18, v254, 24
	s_nop 0
	v_addc_co_u32_e32 v145, vcc, 0, v173, vcc
	v_add_co_u32_e32 v178, vcc, s2, v172
	s_movk_i32 s2, 0x7000
	s_nop 0
	v_addc_co_u32_e32 v179, vcc, 0, v173, vcc
	v_add_co_u32_e32 v146, vcc, s2, v172
	s_mov_b32 s2, 0xa000
	s_nop 0
	v_addc_co_u32_e32 v147, vcc, 0, v173, vcc
	v_add_co_u32_e32 v180, vcc, s60, v172
	global_load_dwordx4 v[16:19], v[144:145], off offset:-4096 nt
	global_load_dwordx4 v[20:23], v[146:147], off offset:-4096 nt
	v_addc_co_u32_e32 v181, vcc, 0, v173, vcc
	v_add_co_u32_e32 v148, vcc, s68, v172
	v_readlane_b32 s19, v254, 25
	s_nop 0
	v_addc_co_u32_e32 v149, vcc, 0, v173, vcc
	v_add_co_u32_e32 v182, vcc, s2, v172
	s_mov_b32 s2, 0xb000
	s_nop 0
	v_addc_co_u32_e32 v183, vcc, 0, v173, vcc
	v_add_co_u32_e32 v150, vcc, s2, v172
	s_mov_b32 s2, 0xe000
	s_nop 0
	v_addc_co_u32_e32 v151, vcc, 0, v173, vcc
	v_add_co_u32_e32 v184, vcc, s61, v172
	global_load_dwordx4 v[24:27], v[148:149], off offset:-4096 nt
	global_load_dwordx4 v[28:31], v[150:151], off offset:-4096 nt
	v_addc_co_u32_e32 v185, vcc, 0, v173, vcc
	v_add_co_u32_e32 v152, vcc, s69, v172
	v_readlane_b32 s22, v254, 28
	s_nop 0
	v_addc_co_u32_e32 v153, vcc, 0, v173, vcc
	v_add_co_u32_e32 v186, vcc, s2, v172
	s_mov_b32 s2, 0xf000
	s_nop 0
	v_addc_co_u32_e32 v187, vcc, 0, v173, vcc
	v_add_co_u32_e32 v154, vcc, s2, v172
	s_mov_b32 s2, 0x12000
	s_nop 0
	v_addc_co_u32_e32 v155, vcc, 0, v173, vcc
	v_add_co_u32_e32 v188, vcc, s62, v172
	global_load_dwordx4 v[56:59], v[152:153], off offset:-4096 nt
	global_load_dwordx4 v[60:63], v[154:155], off offset:-4096 nt
	v_addc_co_u32_e32 v189, vcc, 0, v173, vcc
	v_add_co_u32_e32 v156, vcc, s88, v172
	v_readlane_b32 s23, v254, 29
	s_nop 0
	v_addc_co_u32_e32 v157, vcc, 0, v173, vcc
	v_add_co_u32_e32 v190, vcc, s2, v172
	s_mov_b32 s2, 0x13000
	s_nop 0
	v_addc_co_u32_e32 v191, vcc, 0, v173, vcc
	v_add_co_u32_e32 v158, vcc, s2, v172
	s_mov_b32 s2, 0x16000
	s_nop 0
	v_addc_co_u32_e32 v159, vcc, 0, v173, vcc
	v_add_co_u32_e32 v192, vcc, s63, v172
	global_load_dwordx4 v[48:51], v[156:157], off offset:-4096 nt
	global_load_dwordx4 v[52:55], v[158:159], off offset:-4096 nt
	v_addc_co_u32_e32 v193, vcc, 0, v173, vcc
	v_add_co_u32_e32 v160, vcc, s89, v172
	v_readlane_b32 s24, v254, 30
	s_nop 0
	v_addc_co_u32_e32 v161, vcc, 0, v173, vcc
	v_add_co_u32_e32 v194, vcc, s2, v172
	s_mov_b32 s2, 0x17000
	s_nop 0
	v_addc_co_u32_e32 v195, vcc, 0, v173, vcc
	v_add_co_u32_e32 v162, vcc, s2, v172
	s_mov_b32 s2, 0x1a000
	s_nop 0
	v_addc_co_u32_e32 v163, vcc, 0, v173, vcc
	v_add_co_u32_e32 v196, vcc, s64, v172
	global_load_dwordx4 v[80:83], v[160:161], off offset:-4096 nt
	global_load_dwordx4 v[84:87], v[162:163], off offset:-4096 nt
	v_addc_co_u32_e32 v197, vcc, 0, v173, vcc
	v_add_co_u32_e32 v164, vcc, s90, v172
	v_readlane_b32 s25, v254, 31
	s_nop 0
	v_addc_co_u32_e32 v165, vcc, 0, v173, vcc
	v_add_co_u32_e32 v198, vcc, s2, v172
	s_mov_b32 s2, 0x1b000
	s_nop 0
	v_addc_co_u32_e32 v199, vcc, 0, v173, vcc
	v_add_co_u32_e32 v166, vcc, s2, v172
	s_mov_b32 s2, 0x1e000
	s_nop 0
	v_addc_co_u32_e32 v167, vcc, 0, v173, vcc
	v_add_co_u32_e32 v200, vcc, s65, v172
	global_load_dwordx4 v[88:91], v[164:165], off offset:-4096 nt
	global_load_dwordx4 v[92:95], v[166:167], off offset:-4096 nt
	v_addc_co_u32_e32 v201, vcc, 0, v173, vcc
	v_add_co_u32_e32 v168, vcc, s91, v172
	v_readlane_b32 s26, v254, 32
	s_nop 0
	v_addc_co_u32_e32 v169, vcc, 0, v173, vcc
	v_add_co_u32_e32 v202, vcc, s2, v172
	s_mov_b32 s2, 0x1f000
	s_nop 0
	v_addc_co_u32_e32 v203, vcc, 0, v173, vcc
	v_add_co_u32_e32 v170, vcc, s2, v172
	v_readlane_b32 s27, v254, 33
	s_nop 0
	v_addc_co_u32_e32 v171, vcc, 0, v173, vcc
	global_load_dwordx4 v[108:111], v[168:169], off offset:-4096 nt
	global_load_dwordx4 v[112:115], v[170:171], off offset:-4096 nt
	global_load_dwordx4 v[116:119], v[142:143], off offset:-4096 nt
	global_load_dwordx4 v[96:99], v128, s[48:49] offset:1024 nt
	global_load_dwordx4 v[100:103], v[174:175], off offset:1024 nt
	global_load_dwordx4 v[104:107], v[176:177], off offset:1024 nt
	global_load_dwordx4 v[124:127], v[178:179], off offset:1024 nt
	global_load_dwordx4 v[64:67], v[180:181], off offset:1024 nt
	global_load_dwordx4 v[68:71], v[182:183], off offset:1024 nt
	global_load_dwordx4 v[72:75], v[184:185], off offset:1024 nt
	global_load_dwordx4 v[76:79], v[186:187], off offset:1024 nt
	global_load_dwordx4 v[32:35], v[188:189], off offset:1024 nt
	global_load_dwordx4 v[36:39], v[190:191], off offset:1024 nt
	global_load_dwordx4 v[40:43], v[192:193], off offset:1024 nt
	global_load_dwordx4 v[44:47], v[194:195], off offset:1024 nt
	global_load_dwordx4 v[0:3], v[196:197], off offset:1024 nt
	global_load_dwordx4 v[4:7], v[198:199], off offset:1024 nt
	global_load_dwordx4 v[8:11], v[200:201], off offset:1024 nt
	global_load_dwordx4 v[120:123], v128, s[48:49] nt
	global_load_dwordx4 v[12:15], v[202:203], off offset:1024 nt
	v_readlane_b32 s28, v254, 34
	v_readlane_b32 s29, v254, 35
	v_readlane_b32 s30, v254, 36
	v_readlane_b32 s31, v254, 37
	v_lshl_add_u64 v[140:141], s[50:51], 0, v[130:131]
	s_waitcnt vmcnt(1)
; #define LAS __attribute__((address_space(3)))
; __device__ __forceinline__ unsigned pack4_fp8(float a, float b, float c, float d) { int r = 0; r = __builtin_amdgcn_cvt_pk_fp8_f32(a, b, r, false); r = __builtin_amdgcn_cvt_pk_fp8_f32(c, d, r, true); return (unsigned)r; }
; __device__ __forceinline__ void cvt8_to_lds(const f32x4 (&v)[16], LAS unsigned char* tile, int lane, int wv) {
; #pragma unroll
;     for (int i = 0; i < 4; ++i) { u32x4 w; w.x = pack4_fp8(v[0][i] * W8_SCALE, v[1][i] * W8_SCALE, v[2][i] * W8_SCALE, v[3][i] * W8_SCALE); w.y = pack4_fp8(v[4][i] * W8_SCALE, v[5][i] * W8_SCALE, v[6][i] * W8_SCALE, v[7][i] * W8_SCALE);
;         w.z = pack4_fp8(v[8][i] * W8_SCALE, v[9][i] * W8_SCALE, v[10][i] * W8_SCALE, v[11][i] * W8_SCALE); w.w = pack4_fp8(v[12][i] * W8_SCALE, v[13][i] * W8_SCALE, v[14][i] * W8_SCALE, v[15][i] * W8_SCALE);
;         *(LAS u32x4*)(tile + (4 * lane + i) * 128 + ((wv ^ (lane & 7)) << 4)) = w; }
; }
; __device__ __forceinline__ void cvt8_from_lds(const LAS unsigned char* tile, fp8_t* d, int ld_dst, int tid) {
;     const int c = tid & 7;
; #pragma unroll
;     for (int q = 0; q < 4; ++q) { const int r = (tid >> 3) + 64 * q; const u32x4 w = *(const LAS u32x4*)(tile + r * 128 + ((c ^ ((r >> 2) & 7)) << 4));
;         __builtin_nontemporal_store(w, (u32x4*)(d + (size_t)r * ld_dst + 16 * c)); }
; }
; __device__ __forceinline__ void cvt_item_lds(const float* src, int ld_src, fp8_t* dst, int ld_dst, LAS unsigned char* lds, int tid, int wv) {
;     const int lane = tid & 63;
;     const float* s = src + (size_t)(16 * wv) * ld_src + 4 * lane;
;     f32x4 va[16], vb[16];
;     cvt8_load(va, s, ld_src);
; #pragma unroll
;     for (int t = 0; t < 8; t += 2) {
;         cvt8_load(vb, s + (t + 1) * 256, ld_src); __builtin_amdgcn_sched_barrier(0);
;         cvt8_to_lds(va, lds, lane, wv); CVT_LDS_BAR(); __builtin_amdgcn_sched_barrier(0);
;         cvt8_from_lds(lds, dst + (size_t)(t * 256) * ld_dst, ld_dst, tid); __builtin_amdgcn_sched_barrier(0);
;         if (t + 2 < 8) { cvt8_load(va, s + (t + 2) * 256, ld_src); __builtin_amdgcn_sched_barrier(0); }
;         cvt8_to_lds(vb, lds + 32768, lane, wv); CVT_LDS_BAR(); __builtin_amdgcn_sched_barrier(0);
;         cvt8_from_lds(lds + 32768, dst + (size_t)((t + 1) * 256) * ld_dst, ld_dst, tid); __builtin_amdgcn_sched_barrier(0);
;     }
	v_mul_f32_e32 v120, 0x42800000, v120
	v_mul_f32_e32 v116, 0x42800000, v116
	v_mov_b32_e32 v210, v129
	v_cvt_pk_fp8_f32 v210, v120, v116
	v_mul_f32_e32 v16, 0x42800000, v16
	v_mul_f32_e32 v20, 0x42800000, v20
	v_mov_b32_e32 v211, v129
	v_cvt_pk_fp8_f32 v210, v16, v20 op_sel:[0,0,1]
	v_mul_f32_e32 v16, 0x42800000, v24
	v_mul_f32_e32 v20, 0x42800000, v28
	v_cvt_pk_fp8_f32 v211, v16, v20
	v_mul_f32_e32 v16, 0x42800000, v48
	v_mul_f32_e32 v20, 0x42800000, v52
	v_mov_b32_e32 v212, v129
	v_cvt_pk_fp8_f32 v212, v16, v20
	v_mul_f32_e32 v16, 0x42800000, v88
	v_mul_f32_e32 v20, 0x42800000, v92
	v_mov_b32_e32 v213, v129
	v_cvt_pk_fp8_f32 v213, v16, v20
	v_mul_f32_e32 v24, 0x42800000, v56
	v_mul_f32_e32 v28, 0x42800000, v60
	v_cvt_pk_fp8_f32 v211, v24, v28 op_sel:[0,0,1]
	v_mul_f32_e32 v24, 0x42800000, v80
	v_mul_f32_e32 v28, 0x42800000, v84
	v_cvt_pk_fp8_f32 v212, v24, v28 op_sel:[0,0,1]
	v_mul_f32_e32 v24, 0x42800000, v108
	v_mul_f32_e32 v28, 0x42800000, v112
	v_cvt_pk_fp8_f32 v213, v24, v28 op_sel:[0,0,1]
	v_mul_f32_e32 v16, 0x42800000, v121
	v_mul_f32_e32 v20, 0x42800000, v117
	v_mul_f32_e32 v17, 0x42800000, v17
	ds_write_b128 v204, v[210:213]
	v_mov_b32_e32 v210, v129
	v_cvt_pk_fp8_f32 v210, v16, v20
	v_mul_f32_e32 v21, 0x42800000, v21
	v_mul_f32_e32 v16, 0x42800000, v25
	v_mov_b32_e32 v211, v129
	v_cvt_pk_fp8_f32 v210, v17, v21 op_sel:[0,0,1]
	v_mul_f32_e32 v17, 0x42800000, v29
	v_cvt_pk_fp8_f32 v211, v16, v17
	v_mul_f32_e32 v16, 0x42800000, v49
	v_mul_f32_e32 v17, 0x42800000, v53
	v_mov_b32_e32 v212, v129
	v_cvt_pk_fp8_f32 v212, v16, v17
	v_mul_f32_e32 v16, 0x42800000, v89
	v_mul_f32_e32 v17, 0x42800000, v93
	v_mov_b32_e32 v213, v129
	v_cvt_pk_fp8_f32 v213, v16, v17
	v_mul_f32_e32 v20, 0x42800000, v57
	v_mul_f32_e32 v21, 0x42800000, v61
	v_cvt_pk_fp8_f32 v211, v20, v21 op_sel:[0,0,1]
	v_mul_f32_e32 v20, 0x42800000, v81
	v_mul_f32_e32 v21, 0x42800000, v85
	v_cvt_pk_fp8_f32 v212, v20, v21 op_sel:[0,0,1]
	v_mul_f32_e32 v20, 0x42800000, v109
	v_mul_f32_e32 v21, 0x42800000, v113
	v_cvt_pk_fp8_f32 v213, v20, v21 op_sel:[0,0,1]
	v_mul_f32_e32 v16, 0x42800000, v122
	v_mul_f32_e32 v17, 0x42800000, v118
	v_mul_f32_e32 v18, 0x42800000, v18
	ds_write_b128 v204, v[210:213] offset:128
	v_mov_b32_e32 v210, v129
	v_cvt_pk_fp8_f32 v210, v16, v17
	v_mul_f32_e32 v16, 0x42800000, v26
	v_mul_f32_e32 v17, 0x42800000, v30
	v_mov_b32_e32 v211, v129
	v_cvt_pk_fp8_f32 v211, v16, v17
	v_mul_f32_e32 v16, 0x42800000, v50
	v_mul_f32_e32 v17, 0x42800000, v54
	v_mov_b32_e32 v212, v129
	v_cvt_pk_fp8_f32 v212, v16, v17
	v_mul_f32_e32 v16, 0x42800000, v90
	v_mul_f32_e32 v17, 0x42800000, v94
	v_mov_b32_e32 v213, v129
	v_mul_f32_e32 v20, 0x42800000, v22
	v_cvt_pk_fp8_f32 v213, v16, v17
	v_cvt_pk_fp8_f32 v210, v18, v20 op_sel:[0,0,1]
	v_mul_f32_e32 v18, 0x42800000, v58
	v_mul_f32_e32 v20, 0x42800000, v62
	v_cvt_pk_fp8_f32 v211, v18, v20 op_sel:[0,0,1]
	v_mul_f32_e32 v18, 0x42800000, v82
	v_mul_f32_e32 v20, 0x42800000, v86
	v_cvt_pk_fp8_f32 v212, v18, v20 op_sel:[0,0,1]
	v_mul_f32_e32 v18, 0x42800000, v110
	v_mul_f32_e32 v20, 0x42800000, v114
	v_cvt_pk_fp8_f32 v213, v18, v20 op_sel:[0,0,1]
	v_mul_f32_e32 v17, 0x42800000, v123
	v_mul_f32_e32 v18, 0x42800000, v119
	v_mov_b32_e32 v16, v129
	v_cvt_pk_fp8_f32 v16, v17, v18
	v_mul_f32_e32 v19, 0x42800000, v19
	v_mul_f32_e32 v20, 0x42800000, v23
	v_mul_f32_e32 v18, 0x42800000, v27
	v_cvt_pk_fp8_f32 v16, v19, v20 op_sel:[0,0,1]
	v_mul_f32_e32 v19, 0x42800000, v31
	v_mov_b32_e32 v17, v129
	v_cvt_pk_fp8_f32 v17, v18, v19
	v_mul_f32_e32 v20, 0x42800000, v59
	v_mul_f32_e32 v21, 0x42800000, v63
	v_mul_f32_e32 v19, 0x42800000, v51
	v_cvt_pk_fp8_f32 v17, v20, v21 op_sel:[0,0,1]
	v_mul_f32_e32 v20, 0x42800000, v55
	v_mov_b32_e32 v18, v129
	v_cvt_pk_fp8_f32 v18, v19, v20
	v_mul_f32_e32 v21, 0x42800000, v83
	v_mul_f32_e32 v22, 0x42800000, v87
	v_mul_f32_e32 v20, 0x42800000, v91
	v_cvt_pk_fp8_f32 v18, v21, v22 op_sel:[0,0,1]
	v_mul_f32_e32 v21, 0x42800000, v95
	v_mov_b32_e32 v19, v129
	v_cvt_pk_fp8_f32 v19, v20, v21
	v_mul_f32_e32 v22, 0x42800000, v111
	v_mul_f32_e32 v23, 0x42800000, v115
	ds_write_b128 v204, v[210:213] offset:256
	v_cvt_pk_fp8_f32 v19, v22, v23 op_sel:[0,0,1]
	ds_write_b128 v204, v[16:19] offset:384
	s_waitcnt lgkmcnt(0)
	s_barrier
	ds_read_b128 v[16:19], v205
	v_lshl_add_u64 v[20:21], v[140:141], 0, v[132:133]
	s_waitcnt lgkmcnt(0)
	global_store_dwordx4 v[20:21], v[16:19], off nt
	ds_read_b128 v[16:19], v206
	v_lshl_add_u64 v[20:21], v[140:141], 0, v[134:135]
	s_waitcnt lgkmcnt(0)
	global_store_dwordx4 v[20:21], v[16:19], off nt
	ds_read_b128 v[16:19], v207
	v_lshl_add_u64 v[20:21], v[140:141], 0, v[136:137]
	s_waitcnt lgkmcnt(0)
	global_store_dwordx4 v[20:21], v[16:19], off nt
	ds_read_b128 v[16:19], v208
	v_lshl_add_u64 v[20:21], v[140:141], 0, v[138:139]
	s_waitcnt lgkmcnt(0)
; #define LAS __attribute__((address_space(3)))
; __device__ __forceinline__ unsigned pack4_fp8(float a, float b, float c, float d) { int r = 0; r = __builtin_amdgcn_cvt_pk_fp8_f32(a, b, r, false); r = __builtin_amdgcn_cvt_pk_fp8_f32(c, d, r, true); return (unsigned)r; }
; __device__ __forceinline__ void cvt8_to_lds(const f32x4 (&v)[16], LAS unsigned char* tile, int lane, int wv) {
; #pragma unroll
;     for (int i = 0; i < 4; ++i) { u32x4 w; w.x = pack4_fp8(v[0][i] * W8_SCALE, v[1][i] * W8_SCALE, v[2][i] * W8_SCALE, v[3][i] * W8_SCALE); w.y = pack4_fp8(v[4][i] * W8_SCALE, v[5][i] * W8_SCALE, v[6][i] * W8_SCALE, v[7][i] * W8_SCALE);
;         w.z = pack4_fp8(v[8][i] * W8_SCALE, v[9][i] * W8_SCALE, v[10][i] * W8_SCALE, v[11][i] * W8_SCALE); w.w = pack4_fp8(v[12][i] * W8_SCALE, v[13][i] * W8_SCALE, v[14][i] * W8_SCALE, v[15][i] * W8_SCALE);
;         *(LAS u32x4*)(tile + (4 * lane + i) * 128 + ((wv ^ (lane & 7)) << 4)) = w; }
; }
; __device__ __forceinline__ void cvt8_from_lds(const LAS unsigned char* tile, fp8_t* d, int ld_dst, int tid) {
;     const int c = tid & 7;
; #pragma unroll
;     for (int q = 0; q < 4; ++q) { const int r = (tid >> 3) + 64 * q; const u32x4 w = *(const LAS u32x4*)(tile + r * 128 + ((c ^ ((r >> 2) & 7)) << 4));
;         __builtin_nontemporal_store(w, (u32x4*)(d + (size_t)r * ld_dst + 16 * c)); }
; }
; __device__ __forceinline__ void cvt_item_lds(const float* src, int ld_src, fp8_t* dst, int ld_dst, LAS unsigned char* lds, int tid, int wv) {
;     const int lane = tid & 63;
;     const float* s = src + (size_t)(16 * wv) * ld_src + 4 * lane;
;     f32x4 va[16], vb[16];
;     cvt8_load(va, s, ld_src);
; #pragma unroll
;     for (int t = 0; t < 8; t += 2) {
;         cvt8_load(vb, s + (t + 1) * 256, ld_src); __builtin_amdgcn_sched_barrier(0);
;         cvt8_to_lds(va, lds, lane, wv); CVT_LDS_BAR(); __builtin_amdgcn_sched_barrier(0);
;         cvt8_from_lds(lds, dst + (size_t)(t * 256) * ld_dst, ld_dst, tid); __builtin_amdgcn_sched_barrier(0);
;         if (t + 2 < 8) { cvt8_load(va, s + (t + 2) * 256, ld_src); __builtin_amdgcn_sched_barrier(0); }
;         cvt8_to_lds(vb, lds + 32768, lane, wv); CVT_LDS_BAR(); __builtin_amdgcn_sched_barrier(0);
;         cvt8_from_lds(lds + 32768, dst + (size_t)((t + 1) * 256) * ld_dst, ld_dst, tid); __builtin_amdgcn_sched_barrier(0);
;     }
	global_store_dwordx4 v[20:21], v[16:19], off nt
	global_load_dwordx4 v[108:111], v[174:175], off offset:2048 nt
	global_load_dwordx4 v[112:115], v[176:177], off offset:2048 nt
	global_load_dwordx4 v[116:119], v[178:179], off offset:2048 nt
	global_load_dwordx4 v[80:83], v[180:181], off offset:2048 nt
	global_load_dwordx4 v[84:87], v[182:183], off offset:2048 nt
	global_load_dwordx4 v[88:91], v[184:185], off offset:2048 nt
	global_load_dwordx4 v[92:95], v[186:187], off offset:2048 nt
	global_load_dwordx4 v[48:51], v[188:189], off offset:2048 nt
	global_load_dwordx4 v[52:55], v[190:191], off offset:2048 nt
	global_load_dwordx4 v[56:59], v[192:193], off offset:2048 nt
	global_load_dwordx4 v[60:63], v[194:195], off offset:2048 nt
	global_load_dwordx4 v[16:19], v[196:197], off offset:2048 nt
	global_load_dwordx4 v[20:23], v[198:199], off offset:2048 nt
	global_load_dwordx4 v[24:27], v[200:201], off offset:2048 nt
	global_load_dwordx4 v[120:123], v128, s[48:49] offset:2048 nt
	global_load_dwordx4 v[28:31], v[202:203], off offset:2048 nt
	v_mul_f32_e32 v96, 0x42800000, v96
	v_mul_f32_e32 v100, 0x42800000, v100
	v_mov_b32_e32 v210, v129
	v_mul_f32_e32 v64, 0x42800000, v64
	v_mul_f32_e32 v68, 0x42800000, v68
	v_mov_b32_e32 v211, v129
	v_mul_f32_e32 v32, 0x42800000, v32
	v_mul_f32_e32 v36, 0x42800000, v36
	v_mov_b32_e32 v212, v129
	v_mul_f32_e32 v0, 0x42800000, v0
	v_mul_f32_e32 v4, 0x42800000, v4
	v_mov_b32_e32 v213, v129
	v_cvt_pk_fp8_f32 v210, v96, v100
	v_cvt_pk_fp8_f32 v211, v64, v68
	v_cvt_pk_fp8_f32 v212, v32, v36
	v_cvt_pk_fp8_f32 v213, v0, v4
	v_mul_f32_e32 v104, 0x42800000, v104
	v_mul_f32_e32 v124, 0x42800000, v124
	v_mul_f32_e32 v72, 0x42800000, v72
	v_mul_f32_e32 v76, 0x42800000, v76
	v_mul_f32_e32 v40, 0x42800000, v40
	v_mul_f32_e32 v44, 0x42800000, v44
	v_mul_f32_e32 v8, 0x42800000, v8
	s_waitcnt vmcnt(20)
	v_mul_f32_e32 v12, 0x42800000, v12
	v_cvt_pk_fp8_f32 v210, v104, v124 op_sel:[0,0,1]
	v_cvt_pk_fp8_f32 v211, v72, v76 op_sel:[0,0,1]
	v_cvt_pk_fp8_f32 v212, v40, v44 op_sel:[0,0,1]
	v_cvt_pk_fp8_f32 v213, v8, v12 op_sel:[0,0,1]
	v_mul_f32_e32 v0, 0x42800000, v97
	v_mul_f32_e32 v4, 0x42800000, v101
	v_mul_f32_e32 v8, 0x42800000, v105
	ds_write_b128 v204, v[210:213] offset:32768
	v_mov_b32_e32 v210, v129
	v_cvt_pk_fp8_f32 v210, v0, v4
	v_mul_f32_e32 v0, 0x42800000, v65
	v_mul_f32_e32 v4, 0x42800000, v69
	v_mov_b32_e32 v211, v129
	v_cvt_pk_fp8_f32 v211, v0, v4
	v_mul_f32_e32 v0, 0x42800000, v33
	v_mul_f32_e32 v4, 0x42800000, v37
	v_mov_b32_e32 v212, v129
	v_cvt_pk_fp8_f32 v212, v0, v4
	v_mul_f32_e32 v0, 0x42800000, v1
	v_mul_f32_e32 v1, 0x42800000, v5
	v_mov_b32_e32 v213, v129
	v_cvt_pk_fp8_f32 v213, v0, v1
	v_mul_f32_e32 v12, 0x42800000, v125
	v_cvt_pk_fp8_f32 v210, v8, v12 op_sel:[0,0,1]
	v_mul_f32_e32 v8, 0x42800000, v73
	v_mul_f32_e32 v12, 0x42800000, v77
	v_cvt_pk_fp8_f32 v211, v8, v12 op_sel:[0,0,1]
	v_mul_f32_e32 v8, 0x42800000, v41
	v_mul_f32_e32 v12, 0x42800000, v45
	v_mul_f32_e32 v4, 0x42800000, v9
	v_mul_f32_e32 v5, 0x42800000, v13
	v_cvt_pk_fp8_f32 v212, v8, v12 op_sel:[0,0,1]
	v_cvt_pk_fp8_f32 v213, v4, v5 op_sel:[0,0,1]
	v_mul_f32_e32 v0, 0x42800000, v98
	v_mul_f32_e32 v1, 0x42800000, v102
	v_mul_f32_e32 v4, 0x42800000, v106
	ds_write_b128 v204, v[210:213] offset:32896
	v_mov_b32_e32 v210, v129
	v_cvt_pk_fp8_f32 v210, v0, v1
	v_mul_f32_e32 v0, 0x42800000, v66
	v_mul_f32_e32 v1, 0x42800000, v70
	v_mov_b32_e32 v211, v129
	v_cvt_pk_fp8_f32 v211, v0, v1
	v_mul_f32_e32 v0, 0x42800000, v34
	v_mul_f32_e32 v1, 0x42800000, v38
	v_mov_b32_e32 v212, v129
	v_cvt_pk_fp8_f32 v212, v0, v1
	v_mul_f32_e32 v0, 0x42800000, v2
	v_mul_f32_e32 v1, 0x42800000, v6
	v_mov_b32_e32 v213, v129
	v_mul_f32_e32 v5, 0x42800000, v126
	v_cvt_pk_fp8_f32 v213, v0, v1
	v_cvt_pk_fp8_f32 v210, v4, v5 op_sel:[0,0,1]
	v_mul_f32_e32 v4, 0x42800000, v74
	v_mul_f32_e32 v5, 0x42800000, v78
	v_cvt_pk_fp8_f32 v211, v4, v5 op_sel:[0,0,1]
	v_mul_f32_e32 v4, 0x42800000, v42
	v_mul_f32_e32 v5, 0x42800000, v46
	v_cvt_pk_fp8_f32 v212, v4, v5 op_sel:[0,0,1]
	v_mul_f32_e32 v2, 0x42800000, v10
	v_mul_f32_e32 v4, 0x42800000, v14
	v_cvt_pk_fp8_f32 v213, v2, v4 op_sel:[0,0,1]
	v_mul_f32_e32 v1, 0x42800000, v99
	v_mul_f32_e32 v2, 0x42800000, v103
	v_mov_b32_e32 v0, v129
	v_cvt_pk_fp8_f32 v0, v1, v2
	v_mul_f32_e32 v4, 0x42800000, v107
	v_mul_f32_e32 v5, 0x42800000, v127
	v_mul_f32_e32 v2, 0x42800000, v67
	v_cvt_pk_fp8_f32 v0, v4, v5 op_sel:[0,0,1]
	v_mul_f32_e32 v4, 0x42800000, v71
	v_mov_b32_e32 v1, v129
	v_cvt_pk_fp8_f32 v1, v2, v4
	v_mul_f32_e32 v5, 0x42800000, v75
	v_mul_f32_e32 v6, 0x42800000, v79
	v_mul_f32_e32 v4, 0x42800000, v35
	v_cvt_pk_fp8_f32 v1, v5, v6 op_sel:[0,0,1]
	v_mul_f32_e32 v5, 0x42800000, v39
	v_mov_b32_e32 v2, v129
	v_cvt_pk_fp8_f32 v2, v4, v5
	v_mul_f32_e32 v4, 0x42800000, v3
	v_mul_f32_e32 v5, 0x42800000, v7
	v_mov_b32_e32 v3, v129
	v_cvt_pk_fp8_f32 v3, v4, v5
	v_mul_f32_e32 v6, 0x42800000, v43
	v_mul_f32_e32 v8, 0x42800000, v47
	v_cvt_pk_fp8_f32 v2, v6, v8 op_sel:[0,0,1]
	v_mul_f32_e32 v6, 0x42800000, v11
	v_mul_f32_e32 v7, 0x42800000, v15
	v_cvt_pk_fp8_f32 v3, v6, v7 op_sel:[0,0,1]
	ds_write_b128 v204, v[210:213] offset:33024
	ds_write_b128 v204, v[0:3] offset:33152
	s_waitcnt lgkmcnt(0)
	s_barrier
; #define LAS __attribute__((address_space(3)))
; __device__ __forceinline__ unsigned pack4_fp8(float a, float b, float c, float d) { int r = 0; r = __builtin_amdgcn_cvt_pk_fp8_f32(a, b, r, false); r = __builtin_amdgcn_cvt_pk_fp8_f32(c, d, r, true); return (unsigned)r; }
; __device__ __forceinline__ void cvt8_to_lds(const f32x4 (&v)[16], LAS unsigned char* tile, int lane, int wv) {
; #pragma unroll
;     for (int i = 0; i < 4; ++i) { u32x4 w; w.x = pack4_fp8(v[0][i] * W8_SCALE, v[1][i] * W8_SCALE, v[2][i] * W8_SCALE, v[3][i] * W8_SCALE); w.y = pack4_fp8(v[4][i] * W8_SCALE, v[5][i] * W8_SCALE, v[6][i] * W8_SCALE, v[7][i] * W8_SCALE);
;         w.z = pack4_fp8(v[8][i] * W8_SCALE, v[9][i] * W8_SCALE, v[10][i] * W8_SCALE, v[11][i] * W8_SCALE); w.w = pack4_fp8(v[12][i] * W8_SCALE, v[13][i] * W8_SCALE, v[14][i] * W8_SCALE, v[15][i] * W8_SCALE);
;         *(LAS u32x4*)(tile + (4 * lane + i) * 128 + ((wv ^ (lane & 7)) << 4)) = w; }
; }
; __device__ __forceinline__ void cvt8_from_lds(const LAS unsigned char* tile, fp8_t* d, int ld_dst, int tid) {
;     const int c = tid & 7;
; #pragma unroll
;     for (int q = 0; q < 4; ++q) { const int r = (tid >> 3) + 64 * q; const u32x4 w = *(const LAS u32x4*)(tile + r * 128 + ((c ^ ((r >> 2) & 7)) << 4));
;         __builtin_nontemporal_store(w, (u32x4*)(d + (size_t)r * ld_dst + 16 * c)); }
; }
; __device__ __forceinline__ void cvt_item_lds(const float* src, int ld_src, fp8_t* dst, int ld_dst, LAS unsigned char* lds, int tid, int wv) {
;     const int lane = tid & 63;
;     const float* s = src + (size_t)(16 * wv) * ld_src + 4 * lane;
;     f32x4 va[16], vb[16];
;     cvt8_load(va, s, ld_src);
; #pragma unroll
;     for (int t = 0; t < 8; t += 2) {
;         cvt8_load(vb, s + (t + 1) * 256, ld_src); __builtin_amdgcn_sched_barrier(0);
;         cvt8_to_lds(va, lds, lane, wv); CVT_LDS_BAR(); __builtin_amdgcn_sched_barrier(0);
;         cvt8_from_lds(lds, dst + (size_t)(t * 256) * ld_dst, ld_dst, tid); __builtin_amdgcn_sched_barrier(0);
;         if (t + 2 < 8) { cvt8_load(va, s + (t + 2) * 256, ld_src); __builtin_amdgcn_sched_barrier(0); }
;         cvt8_to_lds(vb, lds + 32768, lane, wv); CVT_LDS_BAR(); __builtin_amdgcn_sched_barrier(0);
;         cvt8_from_lds(lds + 32768, dst + (size_t)((t + 1) * 256) * ld_dst, ld_dst, tid); __builtin_amdgcn_sched_barrier(0);
;     }
	ds_read_b128 v[0:3], v205 offset:32768
	v_lshl_add_u64 v[4:5], v[140:141], 0, s[8:9]
	v_lshl_add_u64 v[6:7], v[4:5], 0, v[132:133]
	s_waitcnt lgkmcnt(0)
	global_store_dwordx4 v[6:7], v[0:3], off nt
	ds_read_b128 v[0:3], v206 offset:32768
	v_lshl_add_u64 v[6:7], v[4:5], 0, v[134:135]
	s_waitcnt lgkmcnt(0)
	global_store_dwordx4 v[6:7], v[0:3], off nt
	ds_read_b128 v[0:3], v207 offset:32768
	v_lshl_add_u64 v[6:7], v[4:5], 0, v[136:137]
	v_lshl_add_u64 v[4:5], v[4:5], 0, v[138:139]
	s_waitcnt lgkmcnt(0)
	global_store_dwordx4 v[6:7], v[0:3], off nt
	ds_read_b128 v[0:3], v208 offset:32768
	s_waitcnt lgkmcnt(0)
	global_store_dwordx4 v[4:5], v[0:3], off nt
	global_load_dwordx4 v[96:99], v[174:175], off offset:3072 nt
	global_load_dwordx4 v[100:103], v[176:177], off offset:3072 nt
	global_load_dwordx4 v[104:107], v[178:179], off offset:3072 nt
	global_load_dwordx4 v[64:67], v[180:181], off offset:3072 nt
	global_load_dwordx4 v[68:71], v[182:183], off offset:3072 nt
	global_load_dwordx4 v[72:75], v[184:185], off offset:3072 nt
	global_load_dwordx4 v[76:79], v[186:187], off offset:3072 nt
	global_load_dwordx4 v[32:35], v[188:189], off offset:3072 nt
	global_load_dwordx4 v[36:39], v[190:191], off offset:3072 nt
	global_load_dwordx4 v[40:43], v[192:193], off offset:3072 nt
	global_load_dwordx4 v[44:47], v[194:195], off offset:3072 nt
	global_load_dwordx4 v[0:3], v[196:197], off offset:3072 nt
	global_load_dwordx4 v[4:7], v[198:199], off offset:3072 nt
	global_load_dwordx4 v[8:11], v[200:201], off offset:3072 nt
	global_load_dwordx4 v[124:127], v128, s[48:49] offset:3072 nt
	global_load_dwordx4 v[12:15], v[202:203], off offset:3072 nt
	s_waitcnt vmcnt(21)
	v_mul_f32_e32 v120, 0x42800000, v120
	v_mul_f32_e32 v108, 0x42800000, v108
	v_mov_b32_e32 v174, v129
	v_mul_f32_e32 v80, 0x42800000, v80
	v_mul_f32_e32 v84, 0x42800000, v84
	v_mov_b32_e32 v175, v129
	v_mul_f32_e32 v48, 0x42800000, v48
	v_mul_f32_e32 v52, 0x42800000, v52
	v_mov_b32_e32 v176, v129
	v_mul_f32_e32 v16, 0x42800000, v16
	v_mul_f32_e32 v20, 0x42800000, v20
	v_mov_b32_e32 v177, v129
	v_cvt_pk_fp8_f32 v174, v120, v108
	v_cvt_pk_fp8_f32 v175, v80, v84
	v_cvt_pk_fp8_f32 v176, v48, v52
	v_cvt_pk_fp8_f32 v177, v16, v20
	v_mul_f32_e32 v112, 0x42800000, v112
	v_mul_f32_e32 v116, 0x42800000, v116
	v_mul_f32_e32 v88, 0x42800000, v88
	v_mul_f32_e32 v92, 0x42800000, v92
	v_mul_f32_e32 v56, 0x42800000, v56
	v_mul_f32_e32 v60, 0x42800000, v60
	v_mul_f32_e32 v24, 0x42800000, v24
	s_waitcnt vmcnt(20)
	v_mul_f32_e32 v28, 0x42800000, v28
	v_cvt_pk_fp8_f32 v174, v112, v116 op_sel:[0,0,1]
	v_cvt_pk_fp8_f32 v175, v88, v92 op_sel:[0,0,1]
	v_cvt_pk_fp8_f32 v176, v56, v60 op_sel:[0,0,1]
	v_cvt_pk_fp8_f32 v177, v24, v28 op_sel:[0,0,1]
	v_mul_f32_e32 v16, 0x42800000, v121
	v_mul_f32_e32 v20, 0x42800000, v109
	v_mul_f32_e32 v24, 0x42800000, v113
	ds_write_b128 v204, v[174:177]
	v_mov_b32_e32 v174, v129
	v_cvt_pk_fp8_f32 v174, v16, v20
	v_mul_f32_e32 v16, 0x42800000, v81
	v_mul_f32_e32 v20, 0x42800000, v85
	v_mov_b32_e32 v175, v129
	v_cvt_pk_fp8_f32 v175, v16, v20
	v_mul_f32_e32 v16, 0x42800000, v49
	v_mul_f32_e32 v20, 0x42800000, v53
	v_mov_b32_e32 v176, v129
	v_cvt_pk_fp8_f32 v176, v16, v20
	v_mul_f32_e32 v16, 0x42800000, v17
	v_mul_f32_e32 v17, 0x42800000, v21
	v_mov_b32_e32 v177, v129
	v_cvt_pk_fp8_f32 v177, v16, v17
	v_mul_f32_e32 v28, 0x42800000, v117
	v_cvt_pk_fp8_f32 v174, v24, v28 op_sel:[0,0,1]
	v_mul_f32_e32 v24, 0x42800000, v89
	v_mul_f32_e32 v28, 0x42800000, v93
	v_cvt_pk_fp8_f32 v175, v24, v28 op_sel:[0,0,1]
	v_mul_f32_e32 v24, 0x42800000, v57
	v_mul_f32_e32 v28, 0x42800000, v61
	v_mul_f32_e32 v20, 0x42800000, v25
	v_mul_f32_e32 v21, 0x42800000, v29
	v_cvt_pk_fp8_f32 v176, v24, v28 op_sel:[0,0,1]
	v_cvt_pk_fp8_f32 v177, v20, v21 op_sel:[0,0,1]
	v_mul_f32_e32 v16, 0x42800000, v122
	v_mul_f32_e32 v17, 0x42800000, v110
	v_mul_f32_e32 v20, 0x42800000, v114
	ds_write_b128 v204, v[174:177] offset:128
	v_mov_b32_e32 v174, v129
	v_cvt_pk_fp8_f32 v174, v16, v17
	v_mul_f32_e32 v16, 0x42800000, v82
	v_mul_f32_e32 v17, 0x42800000, v86
	v_mov_b32_e32 v175, v129
	v_cvt_pk_fp8_f32 v175, v16, v17
	v_mul_f32_e32 v16, 0x42800000, v50
	v_mul_f32_e32 v17, 0x42800000, v54
	v_mov_b32_e32 v176, v129
	v_cvt_pk_fp8_f32 v176, v16, v17
	v_mul_f32_e32 v16, 0x42800000, v18
	v_mul_f32_e32 v17, 0x42800000, v22
	v_mov_b32_e32 v177, v129
	v_mul_f32_e32 v21, 0x42800000, v118
	v_cvt_pk_fp8_f32 v177, v16, v17
	v_cvt_pk_fp8_f32 v174, v20, v21 op_sel:[0,0,1]
	v_mul_f32_e32 v20, 0x42800000, v90
	v_mul_f32_e32 v21, 0x42800000, v94
	v_cvt_pk_fp8_f32 v175, v20, v21 op_sel:[0,0,1]
	v_mul_f32_e32 v20, 0x42800000, v58
	v_mul_f32_e32 v21, 0x42800000, v62
	v_cvt_pk_fp8_f32 v176, v20, v21 op_sel:[0,0,1]
	v_mul_f32_e32 v18, 0x42800000, v26
	v_mul_f32_e32 v20, 0x42800000, v30
	v_cvt_pk_fp8_f32 v177, v18, v20 op_sel:[0,0,1]
	v_mul_f32_e32 v17, 0x42800000, v123
	v_mul_f32_e32 v18, 0x42800000, v111
	v_mov_b32_e32 v16, v129
	v_cvt_pk_fp8_f32 v16, v17, v18
	v_mul_f32_e32 v20, 0x42800000, v115
	v_mul_f32_e32 v21, 0x42800000, v119
	v_mul_f32_e32 v18, 0x42800000, v83
	v_cvt_pk_fp8_f32 v16, v20, v21 op_sel:[0,0,1]
	v_mul_f32_e32 v20, 0x42800000, v87
	v_mov_b32_e32 v17, v129
	v_cvt_pk_fp8_f32 v17, v18, v20
	v_mul_f32_e32 v21, 0x42800000, v91
	v_mul_f32_e32 v22, 0x42800000, v95
	v_mul_f32_e32 v20, 0x42800000, v51
	v_cvt_pk_fp8_f32 v17, v21, v22 op_sel:[0,0,1]
	v_mul_f32_e32 v21, 0x42800000, v55
	v_mov_b32_e32 v18, v129
	v_cvt_pk_fp8_f32 v18, v20, v21
	v_mul_f32_e32 v20, 0x42800000, v19
	v_mul_f32_e32 v21, 0x42800000, v23
	v_mov_b32_e32 v19, v129
	v_cvt_pk_fp8_f32 v19, v20, v21
	v_mul_f32_e32 v22, 0x42800000, v59
	v_mul_f32_e32 v24, 0x42800000, v63
	v_cvt_pk_fp8_f32 v18, v22, v24 op_sel:[0,0,1]
	v_mul_f32_e32 v22, 0x42800000, v27
	v_mul_f32_e32 v23, 0x42800000, v31
	v_cvt_pk_fp8_f32 v19, v22, v23 op_sel:[0,0,1]
	ds_write_b128 v204, v[174:177] offset:256
	ds_write_b128 v204, v[16:19] offset:384
	s_waitcnt lgkmcnt(0)
	s_barrier
; #define LAS __attribute__((address_space(3)))
; __device__ __forceinline__ unsigned pack4_fp8(float a, float b, float c, float d) { int r = 0; r = __builtin_amdgcn_cvt_pk_fp8_f32(a, b, r, false); r = __builtin_amdgcn_cvt_pk_fp8_f32(c, d, r, true); return (unsigned)r; }
; __device__ __forceinline__ void cvt8_to_lds(const f32x4 (&v)[16], LAS unsigned char* tile, int lane, int wv) {
; #pragma unroll
;     for (int i = 0; i < 4; ++i) { u32x4 w; w.x = pack4_fp8(v[0][i] * W8_SCALE, v[1][i] * W8_SCALE, v[2][i] * W8_SCALE, v[3][i] * W8_SCALE); w.y = pack4_fp8(v[4][i] * W8_SCALE, v[5][i] * W8_SCALE, v[6][i] * W8_SCALE, v[7][i] * W8_SCALE);
;         w.z = pack4_fp8(v[8][i] * W8_SCALE, v[9][i] * W8_SCALE, v[10][i] * W8_SCALE, v[11][i] * W8_SCALE); w.w = pack4_fp8(v[12][i] * W8_SCALE, v[13][i] * W8_SCALE, v[14][i] * W8_SCALE, v[15][i] * W8_SCALE);
;         *(LAS u32x4*)(tile + (4 * lane + i) * 128 + ((wv ^ (lane & 7)) << 4)) = w; }
; }
; __device__ __forceinline__ void cvt8_from_lds(const LAS unsigned char* tile, fp8_t* d, int ld_dst, int tid) {
;     const int c = tid & 7;
; #pragma unroll
;     for (int q = 0; q < 4; ++q) { const int r = (tid >> 3) + 64 * q; const u32x4 w = *(const LAS u32x4*)(tile + r * 128 + ((c ^ ((r >> 2) & 7)) << 4));
;         __builtin_nontemporal_store(w, (u32x4*)(d + (size_t)r * ld_dst + 16 * c)); }
; }
; __device__ __forceinline__ void cvt_item_lds(const float* src, int ld_src, fp8_t* dst, int ld_dst, LAS unsigned char* lds, int tid, int wv) {
;     const int lane = tid & 63;
;     const float* s = src + (size_t)(16 * wv) * ld_src + 4 * lane;
;     f32x4 va[16], vb[16];
;     cvt8_load(va, s, ld_src);
; #pragma unroll
;     for (int t = 0; t < 8; t += 2) {
;         cvt8_load(vb, s + (t + 1) * 256, ld_src); __builtin_amdgcn_sched_barrier(0);
;         cvt8_to_lds(va, lds, lane, wv); CVT_LDS_BAR(); __builtin_amdgcn_sched_barrier(0);
;         cvt8_from_lds(lds, dst + (size_t)(t * 256) * ld_dst, ld_dst, tid); __builtin_amdgcn_sched_barrier(0);
;         if (t + 2 < 8) { cvt8_load(va, s + (t + 2) * 256, ld_src); __builtin_amdgcn_sched_barrier(0); }
;         cvt8_to_lds(vb, lds + 32768, lane, wv); CVT_LDS_BAR(); __builtin_amdgcn_sched_barrier(0);
;         cvt8_from_lds(lds + 32768, dst + (size_t)((t + 1) * 256) * ld_dst, ld_dst, tid); __builtin_amdgcn_sched_barrier(0);
;     }
	ds_read_b128 v[16:19], v205
	v_lshl_add_u64 v[20:21], v[140:141], 0, s[10:11]
	v_lshl_add_u64 v[22:23], v[20:21], 0, v[132:133]
	s_waitcnt lgkmcnt(0)
	global_store_dwordx4 v[22:23], v[16:19], off nt
	ds_read_b128 v[16:19], v206
	v_lshl_add_u64 v[22:23], v[20:21], 0, v[134:135]
	s_waitcnt lgkmcnt(0)
	global_store_dwordx4 v[22:23], v[16:19], off nt
	ds_read_b128 v[16:19], v207
	v_lshl_add_u64 v[22:23], v[20:21], 0, v[136:137]
	v_lshl_add_u64 v[20:21], v[20:21], 0, v[138:139]
	s_waitcnt lgkmcnt(0)
	global_store_dwordx4 v[22:23], v[16:19], off nt
	ds_read_b128 v[16:19], v208
	s_waitcnt lgkmcnt(0)
	global_store_dwordx4 v[20:21], v[16:19], off nt
	v_add_co_u32_e32 v172, vcc, s66, v172
	s_nop 1
	v_addc_co_u32_e32 v173, vcc, 0, v173, vcc
	global_load_dwordx4 v[108:111], v[172:173], off nt
	global_load_dwordx4 v[112:115], v[142:143], off nt
	global_load_dwordx4 v[116:119], v[144:145], off nt
	global_load_dwordx4 v[120:123], v[146:147], off nt
	global_load_dwordx4 v[80:83], v[148:149], off nt
	global_load_dwordx4 v[84:87], v[150:151], off nt
	global_load_dwordx4 v[88:91], v[152:153], off nt
	global_load_dwordx4 v[92:95], v[154:155], off nt
	global_load_dwordx4 v[48:51], v[156:157], off nt
	global_load_dwordx4 v[52:55], v[158:159], off nt
	global_load_dwordx4 v[56:59], v[160:161], off nt
	global_load_dwordx4 v[60:63], v[162:163], off nt
	global_load_dwordx4 v[16:19], v[164:165], off nt
	global_load_dwordx4 v[20:23], v[166:167], off nt
	global_load_dwordx4 v[24:27], v[168:169], off nt
	global_load_dwordx4 v[28:31], v[170:171], off nt
	s_waitcnt vmcnt(21)
	v_mul_f32_e32 v124, 0x42800000, v124
	v_mul_f32_e32 v96, 0x42800000, v96
	v_mov_b32_e32 v174, v129
	v_mul_f32_e32 v64, 0x42800000, v64
	v_mul_f32_e32 v68, 0x42800000, v68
	v_mov_b32_e32 v175, v129
	v_mul_f32_e32 v32, 0x42800000, v32
	v_mul_f32_e32 v36, 0x42800000, v36
	v_mov_b32_e32 v176, v129
	v_mul_f32_e32 v0, 0x42800000, v0
	v_mul_f32_e32 v4, 0x42800000, v4
	v_mov_b32_e32 v177, v129
	v_cvt_pk_fp8_f32 v174, v124, v96
	v_cvt_pk_fp8_f32 v175, v64, v68
	v_cvt_pk_fp8_f32 v176, v32, v36
	v_cvt_pk_fp8_f32 v177, v0, v4
	v_mul_f32_e32 v100, 0x42800000, v100
	v_mul_f32_e32 v104, 0x42800000, v104
	v_mul_f32_e32 v72, 0x42800000, v72
	v_mul_f32_e32 v76, 0x42800000, v76
	v_mul_f32_e32 v40, 0x42800000, v40
	v_mul_f32_e32 v44, 0x42800000, v44
	v_mul_f32_e32 v8, 0x42800000, v8
	s_waitcnt vmcnt(20)
	v_mul_f32_e32 v12, 0x42800000, v12
	v_cvt_pk_fp8_f32 v174, v100, v104 op_sel:[0,0,1]
	v_cvt_pk_fp8_f32 v175, v72, v76 op_sel:[0,0,1]
	v_cvt_pk_fp8_f32 v176, v40, v44 op_sel:[0,0,1]
	v_cvt_pk_fp8_f32 v177, v8, v12 op_sel:[0,0,1]
	v_mul_f32_e32 v0, 0x42800000, v125
	v_mul_f32_e32 v4, 0x42800000, v97
	v_mul_f32_e32 v8, 0x42800000, v101
	ds_write_b128 v204, v[174:177] offset:32768
	v_mov_b32_e32 v174, v129
	v_cvt_pk_fp8_f32 v174, v0, v4
	v_mul_f32_e32 v0, 0x42800000, v65
	v_mul_f32_e32 v4, 0x42800000, v69
	v_mov_b32_e32 v175, v129
	v_cvt_pk_fp8_f32 v175, v0, v4
	v_mul_f32_e32 v0, 0x42800000, v33
	v_mul_f32_e32 v4, 0x42800000, v37
	v_mov_b32_e32 v176, v129
	v_cvt_pk_fp8_f32 v176, v0, v4
	v_mul_f32_e32 v0, 0x42800000, v1
	v_mul_f32_e32 v1, 0x42800000, v5
	v_mov_b32_e32 v177, v129
	v_cvt_pk_fp8_f32 v177, v0, v1
	v_mul_f32_e32 v12, 0x42800000, v105
	v_cvt_pk_fp8_f32 v174, v8, v12 op_sel:[0,0,1]
	v_mul_f32_e32 v8, 0x42800000, v73
	v_mul_f32_e32 v12, 0x42800000, v77
	v_cvt_pk_fp8_f32 v175, v8, v12 op_sel:[0,0,1]
	v_mul_f32_e32 v8, 0x42800000, v41
	v_mul_f32_e32 v12, 0x42800000, v45
	v_mul_f32_e32 v4, 0x42800000, v9
	v_mul_f32_e32 v5, 0x42800000, v13
	v_cvt_pk_fp8_f32 v176, v8, v12 op_sel:[0,0,1]
	v_cvt_pk_fp8_f32 v177, v4, v5 op_sel:[0,0,1]
	v_mul_f32_e32 v0, 0x42800000, v126
	v_mul_f32_e32 v1, 0x42800000, v98
	v_mul_f32_e32 v4, 0x42800000, v102
	ds_write_b128 v204, v[174:177] offset:32896
	v_mov_b32_e32 v174, v129
	v_cvt_pk_fp8_f32 v174, v0, v1
	v_mul_f32_e32 v0, 0x42800000, v66
	v_mul_f32_e32 v1, 0x42800000, v70
	v_mov_b32_e32 v175, v129
	v_cvt_pk_fp8_f32 v175, v0, v1
	v_mul_f32_e32 v0, 0x42800000, v34
	v_mul_f32_e32 v1, 0x42800000, v38
	v_mov_b32_e32 v176, v129
	v_cvt_pk_fp8_f32 v176, v0, v1
	v_mul_f32_e32 v0, 0x42800000, v2
	v_mul_f32_e32 v1, 0x42800000, v6
	v_mov_b32_e32 v177, v129
	v_mul_f32_e32 v5, 0x42800000, v106
	v_cvt_pk_fp8_f32 v177, v0, v1
	v_cvt_pk_fp8_f32 v174, v4, v5 op_sel:[0,0,1]
	v_mul_f32_e32 v4, 0x42800000, v74
	v_mul_f32_e32 v5, 0x42800000, v78
	v_cvt_pk_fp8_f32 v175, v4, v5 op_sel:[0,0,1]
	v_mul_f32_e32 v4, 0x42800000, v42
	v_mul_f32_e32 v5, 0x42800000, v46
	v_cvt_pk_fp8_f32 v176, v4, v5 op_sel:[0,0,1]
	v_mul_f32_e32 v2, 0x42800000, v10
	v_mul_f32_e32 v4, 0x42800000, v14
	v_cvt_pk_fp8_f32 v177, v2, v4 op_sel:[0,0,1]
	v_mul_f32_e32 v1, 0x42800000, v127
	v_mul_f32_e32 v2, 0x42800000, v99
	v_mov_b32_e32 v0, v129
	v_cvt_pk_fp8_f32 v0, v1, v2
	v_mul_f32_e32 v4, 0x42800000, v103
	v_mul_f32_e32 v5, 0x42800000, v107
	v_mul_f32_e32 v2, 0x42800000, v67
	v_cvt_pk_fp8_f32 v0, v4, v5 op_sel:[0,0,1]
	v_mul_f32_e32 v4, 0x42800000, v71
	v_mov_b32_e32 v1, v129
	v_cvt_pk_fp8_f32 v1, v2, v4
	v_mul_f32_e32 v5, 0x42800000, v75
	v_mul_f32_e32 v6, 0x42800000, v79
	v_mul_f32_e32 v4, 0x42800000, v35
	v_cvt_pk_fp8_f32 v1, v5, v6 op_sel:[0,0,1]
	v_mul_f32_e32 v5, 0x42800000, v39
	v_mov_b32_e32 v2, v129
	v_cvt_pk_fp8_f32 v2, v4, v5
	v_mul_f32_e32 v4, 0x42800000, v3
	v_mul_f32_e32 v5, 0x42800000, v7
	v_mov_b32_e32 v3, v129
	v_cvt_pk_fp8_f32 v3, v4, v5
	v_mul_f32_e32 v6, 0x42800000, v43
	v_mul_f32_e32 v8, 0x42800000, v47
	v_cvt_pk_fp8_f32 v2, v6, v8 op_sel:[0,0,1]
	v_mul_f32_e32 v6, 0x42800000, v11
	v_mul_f32_e32 v7, 0x42800000, v15
	v_cvt_pk_fp8_f32 v3, v6, v7 op_sel:[0,0,1]
	ds_write_b128 v204, v[174:177] offset:33024
	ds_write_b128 v204, v[0:3] offset:33152
	s_waitcnt lgkmcnt(0)
	s_barrier
; #define LAS __attribute__((address_space(3)))
; __device__ __forceinline__ unsigned pack4_fp8(float a, float b, float c, float d) { int r = 0; r = __builtin_amdgcn_cvt_pk_fp8_f32(a, b, r, false); r = __builtin_amdgcn_cvt_pk_fp8_f32(c, d, r, true); return (unsigned)r; }
; __device__ __forceinline__ void cvt8_to_lds(const f32x4 (&v)[16], LAS unsigned char* tile, int lane, int wv) {
; #pragma unroll
;     for (int i = 0; i < 4; ++i) { u32x4 w; w.x = pack4_fp8(v[0][i] * W8_SCALE, v[1][i] * W8_SCALE, v[2][i] * W8_SCALE, v[3][i] * W8_SCALE); w.y = pack4_fp8(v[4][i] * W8_SCALE, v[5][i] * W8_SCALE, v[6][i] * W8_SCALE, v[7][i] * W8_SCALE);
;         w.z = pack4_fp8(v[8][i] * W8_SCALE, v[9][i] * W8_SCALE, v[10][i] * W8_SCALE, v[11][i] * W8_SCALE); w.w = pack4_fp8(v[12][i] * W8_SCALE, v[13][i] * W8_SCALE, v[14][i] * W8_SCALE, v[15][i] * W8_SCALE);
;         *(LAS u32x4*)(tile + (4 * lane + i) * 128 + ((wv ^ (lane & 7)) << 4)) = w; }
; }
; __device__ __forceinline__ void cvt8_from_lds(const LAS unsigned char* tile, fp8_t* d, int ld_dst, int tid) {
;     const int c = tid & 7;
; #pragma unroll
;     for (int q = 0; q < 4; ++q) { const int r = (tid >> 3) + 64 * q; const u32x4 w = *(const LAS u32x4*)(tile + r * 128 + ((c ^ ((r >> 2) & 7)) << 4));
;         __builtin_nontemporal_store(w, (u32x4*)(d + (size_t)r * ld_dst + 16 * c)); }
; }
; __device__ __forceinline__ void cvt_item_lds(const float* src, int ld_src, fp8_t* dst, int ld_dst, LAS unsigned char* lds, int tid, int wv) {
;     const int lane = tid & 63;
;     const float* s = src + (size_t)(16 * wv) * ld_src + 4 * lane;
;     f32x4 va[16], vb[16];
;     cvt8_load(va, s, ld_src);
; #pragma unroll
;     for (int t = 0; t < 8; t += 2) {
;         cvt8_load(vb, s + (t + 1) * 256, ld_src); __builtin_amdgcn_sched_barrier(0);
;         cvt8_to_lds(va, lds, lane, wv); CVT_LDS_BAR(); __builtin_amdgcn_sched_barrier(0);
;         cvt8_from_lds(lds, dst + (size_t)(t * 256) * ld_dst, ld_dst, tid); __builtin_amdgcn_sched_barrier(0);
;         if (t + 2 < 8) { cvt8_load(va, s + (t + 2) * 256, ld_src); __builtin_amdgcn_sched_barrier(0); }
;         cvt8_to_lds(vb, lds + 32768, lane, wv); CVT_LDS_BAR(); __builtin_amdgcn_sched_barrier(0);
;         cvt8_from_lds(lds + 32768, dst + (size_t)((t + 1) * 256) * ld_dst, ld_dst, tid); __builtin_amdgcn_sched_barrier(0);
;     }
	ds_read_b128 v[0:3], v205 offset:32768
	v_lshl_add_u64 v[4:5], v[140:141], 0, s[38:39]
	v_lshl_add_u64 v[6:7], v[4:5], 0, v[132:133]
	s_waitcnt lgkmcnt(0)
	global_store_dwordx4 v[6:7], v[0:3], off nt
	ds_read_b128 v[0:3], v206 offset:32768
	v_lshl_add_u64 v[6:7], v[4:5], 0, v[134:135]
	s_waitcnt lgkmcnt(0)
	global_store_dwordx4 v[6:7], v[0:3], off nt
	ds_read_b128 v[0:3], v207 offset:32768
	v_lshl_add_u64 v[6:7], v[4:5], 0, v[136:137]
	v_lshl_add_u64 v[4:5], v[4:5], 0, v[138:139]
	s_waitcnt lgkmcnt(0)
	global_store_dwordx4 v[6:7], v[0:3], off nt
	ds_read_b128 v[0:3], v208 offset:32768
	s_waitcnt lgkmcnt(0)
	global_store_dwordx4 v[4:5], v[0:3], off nt
	global_load_dwordx4 v[96:99], v[172:173], off offset:1024 nt
	global_load_dwordx4 v[100:103], v[142:143], off offset:1024 nt
	global_load_dwordx4 v[104:107], v[144:145], off offset:1024 nt
	global_load_dwordx4 v[124:127], v[146:147], off offset:1024 nt
	global_load_dwordx4 v[64:67], v[148:149], off offset:1024 nt
	global_load_dwordx4 v[68:71], v[150:151], off offset:1024 nt
	global_load_dwordx4 v[72:75], v[152:153], off offset:1024 nt
	global_load_dwordx4 v[76:79], v[154:155], off offset:1024 nt
	global_load_dwordx4 v[32:35], v[156:157], off offset:1024 nt
	global_load_dwordx4 v[36:39], v[158:159], off offset:1024 nt
	global_load_dwordx4 v[40:43], v[160:161], off offset:1024 nt
	global_load_dwordx4 v[44:47], v[162:163], off offset:1024 nt
	global_load_dwordx4 v[0:3], v[164:165], off offset:1024 nt
	global_load_dwordx4 v[4:7], v[166:167], off offset:1024 nt
	global_load_dwordx4 v[8:11], v[168:169], off offset:1024 nt
	global_load_dwordx4 v[12:15], v[170:171], off offset:1024 nt
	s_waitcnt vmcnt(35)
	v_mul_f32_e32 v108, 0x42800000, v108
	s_waitcnt vmcnt(34)
	v_mul_f32_e32 v112, 0x42800000, v112
	v_mov_b32_e32 v174, v129
	s_waitcnt vmcnt(31)
	v_mul_f32_e32 v80, 0x42800000, v80
	s_waitcnt vmcnt(30)
	v_mul_f32_e32 v84, 0x42800000, v84
	v_mov_b32_e32 v175, v129
	s_waitcnt vmcnt(27)
	v_mul_f32_e32 v48, 0x42800000, v48
	s_waitcnt vmcnt(26)
	v_mul_f32_e32 v52, 0x42800000, v52
	v_mov_b32_e32 v176, v129
	s_waitcnt vmcnt(23)
	v_mul_f32_e32 v16, 0x42800000, v16
	s_waitcnt vmcnt(22)
	v_mul_f32_e32 v20, 0x42800000, v20
	v_mov_b32_e32 v177, v129
	v_cvt_pk_fp8_f32 v174, v108, v112
	v_cvt_pk_fp8_f32 v175, v80, v84
	v_cvt_pk_fp8_f32 v176, v48, v52
	v_cvt_pk_fp8_f32 v177, v16, v20
	v_mul_f32_e32 v116, 0x42800000, v116
	v_mul_f32_e32 v120, 0x42800000, v120
	v_mul_f32_e32 v88, 0x42800000, v88
	v_mul_f32_e32 v92, 0x42800000, v92
	v_mul_f32_e32 v56, 0x42800000, v56
	v_mul_f32_e32 v60, 0x42800000, v60
	s_waitcnt vmcnt(21)
	v_mul_f32_e32 v24, 0x42800000, v24
	s_waitcnt vmcnt(20)
	v_mul_f32_e32 v28, 0x42800000, v28
	v_cvt_pk_fp8_f32 v174, v116, v120 op_sel:[0,0,1]
	v_cvt_pk_fp8_f32 v175, v88, v92 op_sel:[0,0,1]
	v_cvt_pk_fp8_f32 v176, v56, v60 op_sel:[0,0,1]
	v_cvt_pk_fp8_f32 v177, v24, v28 op_sel:[0,0,1]
	v_mul_f32_e32 v16, 0x42800000, v109
	v_mul_f32_e32 v20, 0x42800000, v113
	v_mul_f32_e32 v24, 0x42800000, v117
	ds_write_b128 v204, v[174:177]
	v_mov_b32_e32 v174, v129
	v_cvt_pk_fp8_f32 v174, v16, v20
	v_mul_f32_e32 v16, 0x42800000, v81
	v_mul_f32_e32 v20, 0x42800000, v85
	v_mov_b32_e32 v175, v129
	v_cvt_pk_fp8_f32 v175, v16, v20
	v_mul_f32_e32 v16, 0x42800000, v49
	v_mul_f32_e32 v20, 0x42800000, v53
	v_mov_b32_e32 v176, v129
	v_cvt_pk_fp8_f32 v176, v16, v20
	v_mul_f32_e32 v16, 0x42800000, v17
	v_mul_f32_e32 v17, 0x42800000, v21
	v_mov_b32_e32 v177, v129
	v_cvt_pk_fp8_f32 v177, v16, v17
	v_mul_f32_e32 v28, 0x42800000, v121
	v_cvt_pk_fp8_f32 v174, v24, v28 op_sel:[0,0,1]
	v_mul_f32_e32 v24, 0x42800000, v89
	v_mul_f32_e32 v28, 0x42800000, v93
	v_cvt_pk_fp8_f32 v175, v24, v28 op_sel:[0,0,1]
	v_mul_f32_e32 v24, 0x42800000, v57
	v_mul_f32_e32 v28, 0x42800000, v61
	v_mul_f32_e32 v20, 0x42800000, v25
	v_mul_f32_e32 v21, 0x42800000, v29
	v_cvt_pk_fp8_f32 v176, v24, v28 op_sel:[0,0,1]
	v_cvt_pk_fp8_f32 v177, v20, v21 op_sel:[0,0,1]
	v_mul_f32_e32 v16, 0x42800000, v110
	v_mul_f32_e32 v17, 0x42800000, v114
	v_mul_f32_e32 v20, 0x42800000, v118
	ds_write_b128 v204, v[174:177] offset:128
	v_mov_b32_e32 v174, v129
	v_cvt_pk_fp8_f32 v174, v16, v17
	v_mul_f32_e32 v16, 0x42800000, v82
	v_mul_f32_e32 v17, 0x42800000, v86
	v_mov_b32_e32 v175, v129
	v_cvt_pk_fp8_f32 v175, v16, v17
	v_mul_f32_e32 v16, 0x42800000, v50
	v_mul_f32_e32 v17, 0x42800000, v54
	v_mov_b32_e32 v176, v129
	v_cvt_pk_fp8_f32 v176, v16, v17
	v_mul_f32_e32 v16, 0x42800000, v18
	v_mul_f32_e32 v17, 0x42800000, v22
	v_mov_b32_e32 v177, v129
	v_mul_f32_e32 v21, 0x42800000, v122
	v_cvt_pk_fp8_f32 v177, v16, v17
	v_cvt_pk_fp8_f32 v174, v20, v21 op_sel:[0,0,1]
	v_mul_f32_e32 v20, 0x42800000, v90
	v_mul_f32_e32 v21, 0x42800000, v94
	v_cvt_pk_fp8_f32 v175, v20, v21 op_sel:[0,0,1]
	v_mul_f32_e32 v20, 0x42800000, v58
	v_mul_f32_e32 v21, 0x42800000, v62
	v_cvt_pk_fp8_f32 v176, v20, v21 op_sel:[0,0,1]
	v_mul_f32_e32 v18, 0x42800000, v26
	v_mul_f32_e32 v20, 0x42800000, v30
	v_cvt_pk_fp8_f32 v177, v18, v20 op_sel:[0,0,1]
	v_mul_f32_e32 v17, 0x42800000, v111
	v_mul_f32_e32 v18, 0x42800000, v115
	v_mov_b32_e32 v16, v129
	v_cvt_pk_fp8_f32 v16, v17, v18
	v_mul_f32_e32 v20, 0x42800000, v119
	v_mul_f32_e32 v21, 0x42800000, v123
	v_mul_f32_e32 v18, 0x42800000, v83
	v_cvt_pk_fp8_f32 v16, v20, v21 op_sel:[0,0,1]
	v_mul_f32_e32 v20, 0x42800000, v87
	v_mov_b32_e32 v17, v129
	v_cvt_pk_fp8_f32 v17, v18, v20
	v_mul_f32_e32 v21, 0x42800000, v91
	v_mul_f32_e32 v22, 0x42800000, v95
	v_mul_f32_e32 v20, 0x42800000, v51
	v_cvt_pk_fp8_f32 v17, v21, v22 op_sel:[0,0,1]
	v_mul_f32_e32 v21, 0x42800000, v55
	v_mov_b32_e32 v18, v129
	v_cvt_pk_fp8_f32 v18, v20, v21
	v_mul_f32_e32 v20, 0x42800000, v19
	v_mul_f32_e32 v21, 0x42800000, v23
	v_mov_b32_e32 v19, v129
	v_cvt_pk_fp8_f32 v19, v20, v21
	v_mul_f32_e32 v22, 0x42800000, v59
	v_mul_f32_e32 v24, 0x42800000, v63
	v_cvt_pk_fp8_f32 v18, v22, v24 op_sel:[0,0,1]
	v_mul_f32_e32 v22, 0x42800000, v27
	v_mul_f32_e32 v23, 0x42800000, v31
	v_cvt_pk_fp8_f32 v19, v22, v23 op_sel:[0,0,1]
	ds_write_b128 v204, v[174:177] offset:256
	ds_write_b128 v204, v[16:19] offset:384
	s_waitcnt lgkmcnt(0)
	s_barrier
; #define LAS __attribute__((address_space(3)))
; __device__ __forceinline__ unsigned pack4_fp8(float a, float b, float c, float d) { int r = 0; r = __builtin_amdgcn_cvt_pk_fp8_f32(a, b, r, false); r = __builtin_amdgcn_cvt_pk_fp8_f32(c, d, r, true); return (unsigned)r; }
; __device__ __forceinline__ void cvt8_to_lds(const f32x4 (&v)[16], LAS unsigned char* tile, int lane, int wv) {
; #pragma unroll
;     for (int i = 0; i < 4; ++i) { u32x4 w; w.x = pack4_fp8(v[0][i] * W8_SCALE, v[1][i] * W8_SCALE, v[2][i] * W8_SCALE, v[3][i] * W8_SCALE); w.y = pack4_fp8(v[4][i] * W8_SCALE, v[5][i] * W8_SCALE, v[6][i] * W8_SCALE, v[7][i] * W8_SCALE);
;         w.z = pack4_fp8(v[8][i] * W8_SCALE, v[9][i] * W8_SCALE, v[10][i] * W8_SCALE, v[11][i] * W8_SCALE); w.w = pack4_fp8(v[12][i] * W8_SCALE, v[13][i] * W8_SCALE, v[14][i] * W8_SCALE, v[15][i] * W8_SCALE);
;         *(LAS u32x4*)(tile + (4 * lane + i) * 128 + ((wv ^ (lane & 7)) << 4)) = w; }
; }
; __device__ __forceinline__ void cvt8_from_lds(const LAS unsigned char* tile, fp8_t* d, int ld_dst, int tid) {
;     const int c = tid & 7;
; #pragma unroll
;     for (int q = 0; q < 4; ++q) { const int r = (tid >> 3) + 64 * q; const u32x4 w = *(const LAS u32x4*)(tile + r * 128 + ((c ^ ((r >> 2) & 7)) << 4));
;         __builtin_nontemporal_store(w, (u32x4*)(d + (size_t)r * ld_dst + 16 * c)); }
; }
; __device__ __forceinline__ void cvt_item_lds(const float* src, int ld_src, fp8_t* dst, int ld_dst, LAS unsigned char* lds, int tid, int wv) {
;     const int lane = tid & 63;
;     const float* s = src + (size_t)(16 * wv) * ld_src + 4 * lane;
;     f32x4 va[16], vb[16];
;     cvt8_load(va, s, ld_src);
; #pragma unroll
;     for (int t = 0; t < 8; t += 2) {
;         cvt8_load(vb, s + (t + 1) * 256, ld_src); __builtin_amdgcn_sched_barrier(0);
;         cvt8_to_lds(va, lds, lane, wv); CVT_LDS_BAR(); __builtin_amdgcn_sched_barrier(0);
;         cvt8_from_lds(lds, dst + (size_t)(t * 256) * ld_dst, ld_dst, tid); __builtin_amdgcn_sched_barrier(0);
;         if (t + 2 < 8) { cvt8_load(va, s + (t + 2) * 256, ld_src); __builtin_amdgcn_sched_barrier(0); }
;         cvt8_to_lds(vb, lds + 32768, lane, wv); CVT_LDS_BAR(); __builtin_amdgcn_sched_barrier(0);
;         cvt8_from_lds(lds + 32768, dst + (size_t)((t + 1) * 256) * ld_dst, ld_dst, tid); __builtin_amdgcn_sched_barrier(0);
;     }
	ds_read_b128 v[16:19], v205
	v_lshl_add_u64 v[20:21], v[140:141], 0, s[40:41]
	v_lshl_add_u64 v[22:23], v[20:21], 0, v[132:133]
	s_waitcnt lgkmcnt(0)
	global_store_dwordx4 v[22:23], v[16:19], off nt
	ds_read_b128 v[16:19], v206
	v_lshl_add_u64 v[22:23], v[20:21], 0, v[134:135]
	s_waitcnt lgkmcnt(0)
	global_store_dwordx4 v[22:23], v[16:19], off nt
	ds_read_b128 v[16:19], v207
	v_lshl_add_u64 v[22:23], v[20:21], 0, v[136:137]
	v_lshl_add_u64 v[20:21], v[20:21], 0, v[138:139]
	s_waitcnt lgkmcnt(0)
	global_store_dwordx4 v[22:23], v[16:19], off nt
	ds_read_b128 v[16:19], v208
	s_waitcnt lgkmcnt(0)
	global_store_dwordx4 v[20:21], v[16:19], off nt
	global_load_dwordx4 v[108:111], v[172:173], off offset:2048 nt
	global_load_dwordx4 v[112:115], v[142:143], off offset:2048 nt
	global_load_dwordx4 v[116:119], v[144:145], off offset:2048 nt
	global_load_dwordx4 v[120:123], v[146:147], off offset:2048 nt
	global_load_dwordx4 v[80:83], v[148:149], off offset:2048 nt
	global_load_dwordx4 v[84:87], v[150:151], off offset:2048 nt
	global_load_dwordx4 v[88:91], v[152:153], off offset:2048 nt
	global_load_dwordx4 v[92:95], v[154:155], off offset:2048 nt
	global_load_dwordx4 v[48:51], v[156:157], off offset:2048 nt
	global_load_dwordx4 v[52:55], v[158:159], off offset:2048 nt
	global_load_dwordx4 v[56:59], v[160:161], off offset:2048 nt
	global_load_dwordx4 v[60:63], v[162:163], off offset:2048 nt
	global_load_dwordx4 v[16:19], v[164:165], off offset:2048 nt
	global_load_dwordx4 v[20:23], v[166:167], off offset:2048 nt
	global_load_dwordx4 v[24:27], v[168:169], off offset:2048 nt
	global_load_dwordx4 v[28:31], v[170:171], off offset:2048 nt
	s_waitcnt vmcnt(35)
	v_mul_f32_e32 v96, 0x42800000, v96
	s_waitcnt vmcnt(34)
	v_mul_f32_e32 v100, 0x42800000, v100
	v_mov_b32_e32 v174, v129
	s_waitcnt vmcnt(31)
	v_mul_f32_e32 v64, 0x42800000, v64
	s_waitcnt vmcnt(30)
	v_mul_f32_e32 v68, 0x42800000, v68
	v_mov_b32_e32 v175, v129
	s_waitcnt vmcnt(27)
	v_mul_f32_e32 v32, 0x42800000, v32
	s_waitcnt vmcnt(26)
	v_mul_f32_e32 v36, 0x42800000, v36
	v_mov_b32_e32 v176, v129
	s_waitcnt vmcnt(23)
	v_mul_f32_e32 v0, 0x42800000, v0
	s_waitcnt vmcnt(22)
	v_mul_f32_e32 v4, 0x42800000, v4
	v_mov_b32_e32 v177, v129
	v_cvt_pk_fp8_f32 v174, v96, v100
	v_cvt_pk_fp8_f32 v175, v64, v68
	v_cvt_pk_fp8_f32 v176, v32, v36
	v_cvt_pk_fp8_f32 v177, v0, v4
	v_mul_f32_e32 v104, 0x42800000, v104
	v_mul_f32_e32 v124, 0x42800000, v124
	v_mul_f32_e32 v72, 0x42800000, v72
	v_mul_f32_e32 v76, 0x42800000, v76
	v_mul_f32_e32 v40, 0x42800000, v40
	v_mul_f32_e32 v44, 0x42800000, v44
	s_waitcnt vmcnt(21)
	v_mul_f32_e32 v8, 0x42800000, v8
	s_waitcnt vmcnt(20)
	v_mul_f32_e32 v12, 0x42800000, v12
	v_cvt_pk_fp8_f32 v174, v104, v124 op_sel:[0,0,1]
	v_cvt_pk_fp8_f32 v175, v72, v76 op_sel:[0,0,1]
	v_cvt_pk_fp8_f32 v176, v40, v44 op_sel:[0,0,1]
	v_cvt_pk_fp8_f32 v177, v8, v12 op_sel:[0,0,1]
	v_mul_f32_e32 v0, 0x42800000, v97
	v_mul_f32_e32 v4, 0x42800000, v101
	v_mul_f32_e32 v8, 0x42800000, v105
	ds_write_b128 v204, v[174:177] offset:32768
	v_mov_b32_e32 v174, v129
	v_cvt_pk_fp8_f32 v174, v0, v4
	v_mul_f32_e32 v0, 0x42800000, v65
	v_mul_f32_e32 v4, 0x42800000, v69
	v_mov_b32_e32 v175, v129
	v_cvt_pk_fp8_f32 v175, v0, v4
	v_mul_f32_e32 v0, 0x42800000, v33
	v_mul_f32_e32 v4, 0x42800000, v37
	v_mov_b32_e32 v176, v129
	v_cvt_pk_fp8_f32 v176, v0, v4
	v_mul_f32_e32 v0, 0x42800000, v1
	v_mul_f32_e32 v1, 0x42800000, v5
	v_mov_b32_e32 v177, v129
	v_cvt_pk_fp8_f32 v177, v0, v1
	v_mul_f32_e32 v12, 0x42800000, v125
	v_cvt_pk_fp8_f32 v174, v8, v12 op_sel:[0,0,1]
	v_mul_f32_e32 v8, 0x42800000, v73
	v_mul_f32_e32 v12, 0x42800000, v77
	v_cvt_pk_fp8_f32 v175, v8, v12 op_sel:[0,0,1]
	v_mul_f32_e32 v8, 0x42800000, v41
	v_mul_f32_e32 v12, 0x42800000, v45
	v_mul_f32_e32 v4, 0x42800000, v9
	v_mul_f32_e32 v5, 0x42800000, v13
	v_cvt_pk_fp8_f32 v176, v8, v12 op_sel:[0,0,1]
	v_cvt_pk_fp8_f32 v177, v4, v5 op_sel:[0,0,1]
	v_mul_f32_e32 v0, 0x42800000, v98
	v_mul_f32_e32 v1, 0x42800000, v102
	v_mul_f32_e32 v4, 0x42800000, v106
	ds_write_b128 v204, v[174:177] offset:32896
	v_mov_b32_e32 v174, v129
	v_cvt_pk_fp8_f32 v174, v0, v1
	v_mul_f32_e32 v0, 0x42800000, v66
	v_mul_f32_e32 v1, 0x42800000, v70
	v_mov_b32_e32 v175, v129
	v_cvt_pk_fp8_f32 v175, v0, v1
	v_mul_f32_e32 v0, 0x42800000, v34
	v_mul_f32_e32 v1, 0x42800000, v38
	v_mov_b32_e32 v176, v129
	v_cvt_pk_fp8_f32 v176, v0, v1
	v_mul_f32_e32 v0, 0x42800000, v2
	v_mul_f32_e32 v1, 0x42800000, v6
	v_mov_b32_e32 v177, v129
	v_mul_f32_e32 v5, 0x42800000, v126
	v_cvt_pk_fp8_f32 v177, v0, v1
	v_cvt_pk_fp8_f32 v174, v4, v5 op_sel:[0,0,1]
	v_mul_f32_e32 v4, 0x42800000, v74
	v_mul_f32_e32 v5, 0x42800000, v78
	v_cvt_pk_fp8_f32 v175, v4, v5 op_sel:[0,0,1]
	v_mul_f32_e32 v4, 0x42800000, v42
	v_mul_f32_e32 v5, 0x42800000, v46
	v_cvt_pk_fp8_f32 v176, v4, v5 op_sel:[0,0,1]
	v_mul_f32_e32 v2, 0x42800000, v10
	v_mul_f32_e32 v4, 0x42800000, v14
	v_cvt_pk_fp8_f32 v177, v2, v4 op_sel:[0,0,1]
	v_mul_f32_e32 v1, 0x42800000, v99
	v_mul_f32_e32 v2, 0x42800000, v103
	v_mov_b32_e32 v0, v129
	v_cvt_pk_fp8_f32 v0, v1, v2
	v_mul_f32_e32 v4, 0x42800000, v107
	v_mul_f32_e32 v5, 0x42800000, v127
	v_mul_f32_e32 v2, 0x42800000, v67
	v_cvt_pk_fp8_f32 v0, v4, v5 op_sel:[0,0,1]
	v_mul_f32_e32 v4, 0x42800000, v71
	v_mov_b32_e32 v1, v129
	v_cvt_pk_fp8_f32 v1, v2, v4
	v_mul_f32_e32 v5, 0x42800000, v75
	v_mul_f32_e32 v6, 0x42800000, v79
	v_mul_f32_e32 v4, 0x42800000, v35
	v_cvt_pk_fp8_f32 v1, v5, v6 op_sel:[0,0,1]
	v_mul_f32_e32 v5, 0x42800000, v39
	v_mov_b32_e32 v2, v129
	v_cvt_pk_fp8_f32 v2, v4, v5
	v_mul_f32_e32 v4, 0x42800000, v3
	v_mul_f32_e32 v5, 0x42800000, v7
	v_mov_b32_e32 v3, v129
	v_cvt_pk_fp8_f32 v3, v4, v5
	v_mul_f32_e32 v6, 0x42800000, v43
	v_mul_f32_e32 v8, 0x42800000, v47
	v_cvt_pk_fp8_f32 v2, v6, v8 op_sel:[0,0,1]
	v_mul_f32_e32 v6, 0x42800000, v11
	v_mul_f32_e32 v7, 0x42800000, v15
	v_cvt_pk_fp8_f32 v3, v6, v7 op_sel:[0,0,1]
	ds_write_b128 v204, v[174:177] offset:33024
	ds_write_b128 v204, v[0:3] offset:33152
	s_waitcnt lgkmcnt(0)
	s_barrier
; #define LAS __attribute__((address_space(3)))
; __device__ __forceinline__ unsigned pack4_fp8(float a, float b, float c, float d) { int r = 0; r = __builtin_amdgcn_cvt_pk_fp8_f32(a, b, r, false); r = __builtin_amdgcn_cvt_pk_fp8_f32(c, d, r, true); return (unsigned)r; }
; __device__ __forceinline__ void cvt8_to_lds(const f32x4 (&v)[16], LAS unsigned char* tile, int lane, int wv) {
; #pragma unroll
;     for (int i = 0; i < 4; ++i) { u32x4 w; w.x = pack4_fp8(v[0][i] * W8_SCALE, v[1][i] * W8_SCALE, v[2][i] * W8_SCALE, v[3][i] * W8_SCALE); w.y = pack4_fp8(v[4][i] * W8_SCALE, v[5][i] * W8_SCALE, v[6][i] * W8_SCALE, v[7][i] * W8_SCALE);
;         w.z = pack4_fp8(v[8][i] * W8_SCALE, v[9][i] * W8_SCALE, v[10][i] * W8_SCALE, v[11][i] * W8_SCALE); w.w = pack4_fp8(v[12][i] * W8_SCALE, v[13][i] * W8_SCALE, v[14][i] * W8_SCALE, v[15][i] * W8_SCALE);
;         *(LAS u32x4*)(tile + (4 * lane + i) * 128 + ((wv ^ (lane & 7)) << 4)) = w; }
; }
; __device__ __forceinline__ void cvt8_from_lds(const LAS unsigned char* tile, fp8_t* d, int ld_dst, int tid) {
;     const int c = tid & 7;
; #pragma unroll
;     for (int q = 0; q < 4; ++q) { const int r = (tid >> 3) + 64 * q; const u32x4 w = *(const LAS u32x4*)(tile + r * 128 + ((c ^ ((r >> 2) & 7)) << 4));
;         __builtin_nontemporal_store(w, (u32x4*)(d + (size_t)r * ld_dst + 16 * c)); }
; }
; __device__ __forceinline__ void cvt_item_lds(const float* src, int ld_src, fp8_t* dst, int ld_dst, LAS unsigned char* lds, int tid, int wv) {
;     const int lane = tid & 63;
;     const float* s = src + (size_t)(16 * wv) * ld_src + 4 * lane;
;     f32x4 va[16], vb[16];
;     cvt8_load(va, s, ld_src);
; #pragma unroll
;     for (int t = 0; t < 8; t += 2) {
;         cvt8_load(vb, s + (t + 1) * 256, ld_src); __builtin_amdgcn_sched_barrier(0);
;         cvt8_to_lds(va, lds, lane, wv); CVT_LDS_BAR(); __builtin_amdgcn_sched_barrier(0);
;         cvt8_from_lds(lds, dst + (size_t)(t * 256) * ld_dst, ld_dst, tid); __builtin_amdgcn_sched_barrier(0);
;         if (t + 2 < 8) { cvt8_load(va, s + (t + 2) * 256, ld_src); __builtin_amdgcn_sched_barrier(0); }
;         cvt8_to_lds(vb, lds + 32768, lane, wv); CVT_LDS_BAR(); __builtin_amdgcn_sched_barrier(0);
;         cvt8_from_lds(lds + 32768, dst + (size_t)((t + 1) * 256) * ld_dst, ld_dst, tid); __builtin_amdgcn_sched_barrier(0);
;     }
	ds_read_b128 v[0:3], v205 offset:32768
	v_lshl_add_u64 v[4:5], v[140:141], 0, s[42:43]
	v_lshl_add_u64 v[6:7], v[4:5], 0, v[132:133]
	s_waitcnt lgkmcnt(0)
	global_store_dwordx4 v[6:7], v[0:3], off nt
	ds_read_b128 v[0:3], v206 offset:32768
	v_lshl_add_u64 v[6:7], v[4:5], 0, v[134:135]
	s_waitcnt lgkmcnt(0)
	global_store_dwordx4 v[6:7], v[0:3], off nt
	ds_read_b128 v[0:3], v207 offset:32768
	v_lshl_add_u64 v[6:7], v[4:5], 0, v[136:137]
	v_lshl_add_u64 v[4:5], v[4:5], 0, v[138:139]
	s_waitcnt lgkmcnt(0)
	global_store_dwordx4 v[6:7], v[0:3], off nt
	ds_read_b128 v[0:3], v208 offset:32768
	s_waitcnt lgkmcnt(0)
	global_store_dwordx4 v[4:5], v[0:3], off nt
	global_load_dwordx4 v[96:99], v[172:173], off offset:3072 nt
	global_load_dwordx4 v[100:103], v[142:143], off offset:3072 nt
	global_load_dwordx4 v[104:107], v[144:145], off offset:3072 nt
	global_load_dwordx4 v[124:127], v[146:147], off offset:3072 nt
	global_load_dwordx4 v[64:67], v[148:149], off offset:3072 nt
	global_load_dwordx4 v[68:71], v[150:151], off offset:3072 nt
	global_load_dwordx4 v[72:75], v[152:153], off offset:3072 nt
	global_load_dwordx4 v[76:79], v[154:155], off offset:3072 nt
	global_load_dwordx4 v[32:35], v[156:157], off offset:3072 nt
	global_load_dwordx4 v[36:39], v[158:159], off offset:3072 nt
	global_load_dwordx4 v[40:43], v[160:161], off offset:3072 nt
	global_load_dwordx4 v[44:47], v[162:163], off offset:3072 nt
	global_load_dwordx4 v[0:3], v[164:165], off offset:3072 nt
	global_load_dwordx4 v[4:7], v[166:167], off offset:3072 nt
	global_load_dwordx4 v[8:11], v[168:169], off offset:3072 nt
	global_load_dwordx4 v[12:15], v[170:171], off offset:3072 nt
	s_waitcnt vmcnt(35)
	v_mul_f32_e32 v108, 0x42800000, v108
	s_waitcnt vmcnt(34)
	v_mul_f32_e32 v112, 0x42800000, v112
	v_mov_b32_e32 v142, v129
	s_waitcnt vmcnt(31)
	v_mul_f32_e32 v80, 0x42800000, v80
	s_waitcnt vmcnt(30)
	v_mul_f32_e32 v84, 0x42800000, v84
	v_mov_b32_e32 v143, v129
	s_waitcnt vmcnt(27)
	v_mul_f32_e32 v48, 0x42800000, v48
	s_waitcnt vmcnt(26)
	v_mul_f32_e32 v52, 0x42800000, v52
	v_mov_b32_e32 v144, v129
	s_waitcnt vmcnt(23)
	v_mul_f32_e32 v16, 0x42800000, v16
	s_waitcnt vmcnt(22)
	v_mul_f32_e32 v20, 0x42800000, v20
	v_mov_b32_e32 v145, v129
	v_cvt_pk_fp8_f32 v142, v108, v112
	v_cvt_pk_fp8_f32 v143, v80, v84
	v_cvt_pk_fp8_f32 v144, v48, v52
	v_cvt_pk_fp8_f32 v145, v16, v20
	v_mul_f32_e32 v116, 0x42800000, v116
	v_mul_f32_e32 v120, 0x42800000, v120
	v_mul_f32_e32 v88, 0x42800000, v88
	v_mul_f32_e32 v92, 0x42800000, v92
	v_mul_f32_e32 v56, 0x42800000, v56
	v_mul_f32_e32 v60, 0x42800000, v60
	s_waitcnt vmcnt(21)
	v_mul_f32_e32 v24, 0x42800000, v24
	s_waitcnt vmcnt(20)
	v_mul_f32_e32 v28, 0x42800000, v28
	v_cvt_pk_fp8_f32 v142, v116, v120 op_sel:[0,0,1]
	v_cvt_pk_fp8_f32 v143, v88, v92 op_sel:[0,0,1]
	v_cvt_pk_fp8_f32 v144, v56, v60 op_sel:[0,0,1]
	v_cvt_pk_fp8_f32 v145, v24, v28 op_sel:[0,0,1]
	v_mul_f32_e32 v16, 0x42800000, v109
	v_mul_f32_e32 v20, 0x42800000, v113
	v_mul_f32_e32 v24, 0x42800000, v117
	ds_write_b128 v204, v[142:145]
	v_mov_b32_e32 v142, v129
	v_cvt_pk_fp8_f32 v142, v16, v20
	v_mul_f32_e32 v16, 0x42800000, v81
	v_mul_f32_e32 v20, 0x42800000, v85
	v_mov_b32_e32 v143, v129
	v_cvt_pk_fp8_f32 v143, v16, v20
	v_mul_f32_e32 v16, 0x42800000, v49
	v_mul_f32_e32 v20, 0x42800000, v53
	v_mov_b32_e32 v144, v129
	v_cvt_pk_fp8_f32 v144, v16, v20
	v_mul_f32_e32 v16, 0x42800000, v17
	v_mul_f32_e32 v17, 0x42800000, v21
	v_mov_b32_e32 v145, v129
	v_cvt_pk_fp8_f32 v145, v16, v17
	v_mul_f32_e32 v28, 0x42800000, v121
	v_cvt_pk_fp8_f32 v142, v24, v28 op_sel:[0,0,1]
	v_mul_f32_e32 v24, 0x42800000, v89
	v_mul_f32_e32 v28, 0x42800000, v93
	v_cvt_pk_fp8_f32 v143, v24, v28 op_sel:[0,0,1]
	v_mul_f32_e32 v24, 0x42800000, v57
	v_mul_f32_e32 v28, 0x42800000, v61
	v_mul_f32_e32 v20, 0x42800000, v25
	v_mul_f32_e32 v21, 0x42800000, v29
	v_cvt_pk_fp8_f32 v144, v24, v28 op_sel:[0,0,1]
	v_cvt_pk_fp8_f32 v145, v20, v21 op_sel:[0,0,1]
	v_mul_f32_e32 v16, 0x42800000, v110
	v_mul_f32_e32 v17, 0x42800000, v114
	v_mul_f32_e32 v20, 0x42800000, v118
	ds_write_b128 v204, v[142:145] offset:128
	v_mov_b32_e32 v142, v129
	v_cvt_pk_fp8_f32 v142, v16, v17
	v_mul_f32_e32 v16, 0x42800000, v82
	v_mul_f32_e32 v17, 0x42800000, v86
	v_mov_b32_e32 v143, v129
	v_cvt_pk_fp8_f32 v143, v16, v17
	v_mul_f32_e32 v16, 0x42800000, v50
	v_mul_f32_e32 v17, 0x42800000, v54
	v_mov_b32_e32 v144, v129
	v_cvt_pk_fp8_f32 v144, v16, v17
	v_mul_f32_e32 v16, 0x42800000, v18
	v_mul_f32_e32 v17, 0x42800000, v22
	v_mov_b32_e32 v145, v129
	v_mul_f32_e32 v21, 0x42800000, v122
	v_cvt_pk_fp8_f32 v145, v16, v17
	v_cvt_pk_fp8_f32 v142, v20, v21 op_sel:[0,0,1]
	v_mul_f32_e32 v20, 0x42800000, v90
	v_mul_f32_e32 v21, 0x42800000, v94
	v_cvt_pk_fp8_f32 v143, v20, v21 op_sel:[0,0,1]
	v_mul_f32_e32 v20, 0x42800000, v58
	v_mul_f32_e32 v21, 0x42800000, v62
	v_cvt_pk_fp8_f32 v144, v20, v21 op_sel:[0,0,1]
	v_mul_f32_e32 v18, 0x42800000, v26
	v_mul_f32_e32 v20, 0x42800000, v30
	v_cvt_pk_fp8_f32 v145, v18, v20 op_sel:[0,0,1]
	v_mul_f32_e32 v17, 0x42800000, v111
	v_mul_f32_e32 v18, 0x42800000, v115
	v_mov_b32_e32 v16, v129
	v_cvt_pk_fp8_f32 v16, v17, v18
	v_mul_f32_e32 v20, 0x42800000, v119
	v_mul_f32_e32 v21, 0x42800000, v123
	v_mul_f32_e32 v18, 0x42800000, v83
	v_cvt_pk_fp8_f32 v16, v20, v21 op_sel:[0,0,1]
	v_mul_f32_e32 v20, 0x42800000, v87
	v_mov_b32_e32 v17, v129
	v_cvt_pk_fp8_f32 v17, v18, v20
	v_mul_f32_e32 v21, 0x42800000, v91
	v_mul_f32_e32 v22, 0x42800000, v95
	v_mul_f32_e32 v20, 0x42800000, v51
	v_cvt_pk_fp8_f32 v17, v21, v22 op_sel:[0,0,1]
	v_mul_f32_e32 v21, 0x42800000, v55
	v_mov_b32_e32 v18, v129
	v_cvt_pk_fp8_f32 v18, v20, v21
	v_mul_f32_e32 v20, 0x42800000, v19
	v_mul_f32_e32 v21, 0x42800000, v23
	v_mov_b32_e32 v19, v129
	v_cvt_pk_fp8_f32 v19, v20, v21
	v_mul_f32_e32 v22, 0x42800000, v59
	v_mul_f32_e32 v24, 0x42800000, v63
	v_cvt_pk_fp8_f32 v18, v22, v24 op_sel:[0,0,1]
	v_mul_f32_e32 v22, 0x42800000, v27
	v_mul_f32_e32 v23, 0x42800000, v31
	v_cvt_pk_fp8_f32 v19, v22, v23 op_sel:[0,0,1]
	ds_write_b128 v204, v[142:145] offset:256
	ds_write_b128 v204, v[16:19] offset:384
	s_waitcnt lgkmcnt(0)
	s_barrier
; #define LAS __attribute__((address_space(3)))
; __device__ __forceinline__ unsigned pack4_fp8(float a, float b, float c, float d) { int r = 0; r = __builtin_amdgcn_cvt_pk_fp8_f32(a, b, r, false); r = __builtin_amdgcn_cvt_pk_fp8_f32(c, d, r, true); return (unsigned)r; }
; __device__ __forceinline__ void cvt8_to_lds(const f32x4 (&v)[16], LAS unsigned char* tile, int lane, int wv) {
; #pragma unroll
;     for (int i = 0; i < 4; ++i) { u32x4 w; w.x = pack4_fp8(v[0][i] * W8_SCALE, v[1][i] * W8_SCALE, v[2][i] * W8_SCALE, v[3][i] * W8_SCALE); w.y = pack4_fp8(v[4][i] * W8_SCALE, v[5][i] * W8_SCALE, v[6][i] * W8_SCALE, v[7][i] * W8_SCALE);
;         w.z = pack4_fp8(v[8][i] * W8_SCALE, v[9][i] * W8_SCALE, v[10][i] * W8_SCALE, v[11][i] * W8_SCALE); w.w = pack4_fp8(v[12][i] * W8_SCALE, v[13][i] * W8_SCALE, v[14][i] * W8_SCALE, v[15][i] * W8_SCALE);
;         *(LAS u32x4*)(tile + (4 * lane + i) * 128 + ((wv ^ (lane & 7)) << 4)) = w; }
; }
; __device__ __forceinline__ void cvt8_from_lds(const LAS unsigned char* tile, fp8_t* d, int ld_dst, int tid) {
;     const int c = tid & 7;
; #pragma unroll
;     for (int q = 0; q < 4; ++q) { const int r = (tid >> 3) + 64 * q; const u32x4 w = *(const LAS u32x4*)(tile + r * 128 + ((c ^ ((r >> 2) & 7)) << 4));
;         __builtin_nontemporal_store(w, (u32x4*)(d + (size_t)r * ld_dst + 16 * c)); }
; }
; __device__ __forceinline__ void cvt_item_lds(const float* src, int ld_src, fp8_t* dst, int ld_dst, LAS unsigned char* lds, int tid, int wv) {
;     const int lane = tid & 63;
;     const float* s = src + (size_t)(16 * wv) * ld_src + 4 * lane;
;     f32x4 va[16], vb[16];
;     cvt8_load(va, s, ld_src);
; #pragma unroll
;     for (int t = 0; t < 8; t += 2) {
;         cvt8_load(vb, s + (t + 1) * 256, ld_src); __builtin_amdgcn_sched_barrier(0);
;         cvt8_to_lds(va, lds, lane, wv); CVT_LDS_BAR(); __builtin_amdgcn_sched_barrier(0);
;         cvt8_from_lds(lds, dst + (size_t)(t * 256) * ld_dst, ld_dst, tid); __builtin_amdgcn_sched_barrier(0);
;         if (t + 2 < 8) { cvt8_load(va, s + (t + 2) * 256, ld_src); __builtin_amdgcn_sched_barrier(0); }
;         cvt8_to_lds(vb, lds + 32768, lane, wv); CVT_LDS_BAR(); __builtin_amdgcn_sched_barrier(0);
;         cvt8_from_lds(lds + 32768, dst + (size_t)((t + 1) * 256) * ld_dst, ld_dst, tid); __builtin_amdgcn_sched_barrier(0);
;     }
	ds_read_b128 v[16:19], v205
	v_lshl_add_u64 v[20:21], v[140:141], 0, s[44:45]
	v_lshl_add_u64 v[22:23], v[20:21], 0, v[132:133]
	s_waitcnt lgkmcnt(0)
	global_store_dwordx4 v[22:23], v[16:19], off nt
	ds_read_b128 v[16:19], v206
	v_lshl_add_u64 v[22:23], v[20:21], 0, v[134:135]
	s_waitcnt lgkmcnt(0)
	global_store_dwordx4 v[22:23], v[16:19], off nt
	ds_read_b128 v[16:19], v207
	v_lshl_add_u64 v[22:23], v[20:21], 0, v[136:137]
	v_lshl_add_u64 v[20:21], v[20:21], 0, v[138:139]
	s_waitcnt lgkmcnt(0)
	global_store_dwordx4 v[22:23], v[16:19], off nt
	ds_read_b128 v[16:19], v208
	s_waitcnt lgkmcnt(0)
	global_store_dwordx4 v[20:21], v[16:19], off nt
	s_waitcnt vmcnt(19)
	s_nop 0
	v_mul_f32_e32 v17, 0x42800000, v96
	s_waitcnt vmcnt(18)
	v_mul_f32_e32 v18, 0x42800000, v100
	v_mov_b32_e32 v16, v129
	v_cvt_pk_fp8_f32 v16, v17, v18
	s_waitcnt vmcnt(17)
	v_mul_f32_e32 v19, 0x42800000, v104
	s_waitcnt vmcnt(16)
	v_mul_f32_e32 v20, 0x42800000, v124
	s_waitcnt vmcnt(15)
	v_mul_f32_e32 v18, 0x42800000, v64
	v_cvt_pk_fp8_f32 v16, v19, v20 op_sel:[0,0,1]
	s_waitcnt vmcnt(14)
	v_mul_f32_e32 v19, 0x42800000, v68
	v_mov_b32_e32 v17, v129
	v_cvt_pk_fp8_f32 v17, v18, v19
	s_waitcnt vmcnt(13)
	v_mul_f32_e32 v20, 0x42800000, v72
	s_waitcnt vmcnt(12)
	v_mul_f32_e32 v21, 0x42800000, v76
	s_waitcnt vmcnt(11)
	v_mul_f32_e32 v19, 0x42800000, v32
	v_cvt_pk_fp8_f32 v17, v20, v21 op_sel:[0,0,1]
	s_waitcnt vmcnt(10)
	v_mul_f32_e32 v20, 0x42800000, v36
	v_mov_b32_e32 v18, v129
	v_cvt_pk_fp8_f32 v18, v19, v20
	s_waitcnt vmcnt(7)
	v_mul_f32_e32 v0, 0x42800000, v0
	s_waitcnt vmcnt(6)
	v_mul_f32_e32 v4, 0x42800000, v4
	v_mov_b32_e32 v19, v129
	v_cvt_pk_fp8_f32 v19, v0, v4
	v_mul_f32_e32 v21, 0x42800000, v40
	v_mul_f32_e32 v22, 0x42800000, v44
	s_waitcnt vmcnt(5)
	v_mul_f32_e32 v8, 0x42800000, v8
	s_waitcnt vmcnt(4)
	v_mul_f32_e32 v12, 0x42800000, v12
	v_cvt_pk_fp8_f32 v18, v21, v22 op_sel:[0,0,1]
	v_cvt_pk_fp8_f32 v19, v8, v12 op_sel:[0,0,1]
	v_mul_f32_e32 v0, 0x42800000, v97
	v_mul_f32_e32 v4, 0x42800000, v101
	v_mul_f32_e32 v8, 0x42800000, v105
	ds_write_b128 v204, v[16:19] offset:32768
	v_mov_b32_e32 v16, v129
	v_cvt_pk_fp8_f32 v16, v0, v4
	v_mul_f32_e32 v0, 0x42800000, v65
	v_mul_f32_e32 v4, 0x42800000, v69
	v_mov_b32_e32 v17, v129
	v_cvt_pk_fp8_f32 v17, v0, v4
	v_mul_f32_e32 v0, 0x42800000, v33
	v_mul_f32_e32 v4, 0x42800000, v37
	v_mov_b32_e32 v18, v129
	v_cvt_pk_fp8_f32 v18, v0, v4
	v_mul_f32_e32 v0, 0x42800000, v1
	v_mul_f32_e32 v1, 0x42800000, v5
	v_mov_b32_e32 v19, v129
	v_cvt_pk_fp8_f32 v19, v0, v1
	v_mul_f32_e32 v12, 0x42800000, v125
	v_cvt_pk_fp8_f32 v16, v8, v12 op_sel:[0,0,1]
	v_mul_f32_e32 v8, 0x42800000, v73
	v_mul_f32_e32 v12, 0x42800000, v77
	v_cvt_pk_fp8_f32 v17, v8, v12 op_sel:[0,0,1]
	v_mul_f32_e32 v8, 0x42800000, v41
	v_mul_f32_e32 v12, 0x42800000, v45
	v_mul_f32_e32 v4, 0x42800000, v9
	v_mul_f32_e32 v5, 0x42800000, v13
	v_cvt_pk_fp8_f32 v18, v8, v12 op_sel:[0,0,1]
	v_cvt_pk_fp8_f32 v19, v4, v5 op_sel:[0,0,1]
	v_mul_f32_e32 v0, 0x42800000, v98
	v_mul_f32_e32 v1, 0x42800000, v102
	v_mul_f32_e32 v4, 0x42800000, v106
	ds_write_b128 v204, v[16:19] offset:32896
	v_mov_b32_e32 v16, v129
	v_cvt_pk_fp8_f32 v16, v0, v1
	v_mul_f32_e32 v0, 0x42800000, v66
	v_mul_f32_e32 v1, 0x42800000, v70
	v_mov_b32_e32 v17, v129
	v_cvt_pk_fp8_f32 v17, v0, v1
	v_mul_f32_e32 v0, 0x42800000, v34
	v_mul_f32_e32 v1, 0x42800000, v38
	v_mov_b32_e32 v18, v129
	v_cvt_pk_fp8_f32 v18, v0, v1
	v_mul_f32_e32 v0, 0x42800000, v2
	v_mul_f32_e32 v1, 0x42800000, v6
	v_mov_b32_e32 v19, v129
	v_mul_f32_e32 v5, 0x42800000, v126
	v_cvt_pk_fp8_f32 v19, v0, v1
	v_cvt_pk_fp8_f32 v16, v4, v5 op_sel:[0,0,1]
	v_mul_f32_e32 v4, 0x42800000, v74
	v_mul_f32_e32 v5, 0x42800000, v78
	v_cvt_pk_fp8_f32 v17, v4, v5 op_sel:[0,0,1]
	v_mul_f32_e32 v4, 0x42800000, v42
	v_mul_f32_e32 v5, 0x42800000, v46
	v_cvt_pk_fp8_f32 v18, v4, v5 op_sel:[0,0,1]
	v_mul_f32_e32 v2, 0x42800000, v10
	v_mul_f32_e32 v4, 0x42800000, v14
	v_cvt_pk_fp8_f32 v19, v2, v4 op_sel:[0,0,1]
	v_mul_f32_e32 v1, 0x42800000, v99
	v_mul_f32_e32 v2, 0x42800000, v103
	v_mov_b32_e32 v0, v129
	v_cvt_pk_fp8_f32 v0, v1, v2
	v_mul_f32_e32 v4, 0x42800000, v107
	v_mul_f32_e32 v5, 0x42800000, v127
	v_mul_f32_e32 v2, 0x42800000, v67
	v_cvt_pk_fp8_f32 v0, v4, v5 op_sel:[0,0,1]
	v_mul_f32_e32 v4, 0x42800000, v71
	v_mov_b32_e32 v1, v129
	v_cvt_pk_fp8_f32 v1, v2, v4
	v_mul_f32_e32 v5, 0x42800000, v75
	v_mul_f32_e32 v6, 0x42800000, v79
	v_mul_f32_e32 v4, 0x42800000, v35
	v_cvt_pk_fp8_f32 v1, v5, v6 op_sel:[0,0,1]
	v_mul_f32_e32 v5, 0x42800000, v39
	v_mov_b32_e32 v2, v129
	v_cvt_pk_fp8_f32 v2, v4, v5
	v_mul_f32_e32 v4, 0x42800000, v3
	v_mul_f32_e32 v5, 0x42800000, v7
	v_mov_b32_e32 v3, v129
	v_cvt_pk_fp8_f32 v3, v4, v5
	v_mul_f32_e32 v6, 0x42800000, v43
	v_mul_f32_e32 v8, 0x42800000, v47
	v_cvt_pk_fp8_f32 v2, v6, v8 op_sel:[0,0,1]
	v_mul_f32_e32 v6, 0x42800000, v11
	v_mul_f32_e32 v7, 0x42800000, v15
	v_cvt_pk_fp8_f32 v3, v6, v7 op_sel:[0,0,1]
	ds_write_b128 v204, v[16:19] offset:33024
	ds_write_b128 v204, v[0:3] offset:33152
	s_waitcnt lgkmcnt(0)
	s_barrier
	ds_read_b128 v[0:3], v205 offset:32768
	v_lshl_add_u64 v[4:5], v[140:141], 0, s[46:47]
	v_lshl_add_u64 v[6:7], v[4:5], 0, v[132:133]
	s_waitcnt lgkmcnt(0)
	global_store_dwordx4 v[6:7], v[0:3], off nt
	ds_read_b128 v[0:3], v206 offset:32768
	v_lshl_add_u64 v[6:7], v[4:5], 0, v[134:135]
	s_waitcnt lgkmcnt(0)
	global_store_dwordx4 v[6:7], v[0:3], off nt
	ds_read_b128 v[0:3], v207 offset:32768
	v_lshl_add_u64 v[6:7], v[4:5], 0, v[136:137]
	v_lshl_add_u64 v[4:5], v[4:5], 0, v[138:139]
	s_waitcnt lgkmcnt(0)
	global_store_dwordx4 v[6:7], v[0:3], off nt
	ds_read_b128 v[0:3], v208 offset:32768
	s_waitcnt lgkmcnt(0)
	global_store_dwordx4 v[4:5], v[0:3], off nt
	s_mov_b64 s[48:49], 0

; __device__ __forceinline__ void conv_queue(const Params& p, LAS unsigned char* lds, const int wave, const int cw, const int first, const int last, const int slot_off = LDS_MISC) {
;     ...
;     for (;;) {
;         __syncthreads();
;         if (tid == 0) *slot = first + (int)atomicAdd(&p.ctl[cw], 1u);
;         __syncthreads();
;         const int it = *slot;
;         if (it >= last) break;
.LBB0_1251:
	s_or_b64 exec, exec, s[52:53]
	s_waitcnt vmcnt(0)
	v_readfirstlane_b32 s2, v1
	v_mov_b32_e32 v1, s13
	s_nop 0
	v_add_u32_e32 v0, s2, v0
	v_add_u32_e32 v0, 0x460, v0
	ds_write_b32 v1, v0

; __device__ __forceinline__ void conv_queue(const Params& p, LAS unsigned char* lds, const int wave, const int cw, const int first, const int last, const int slot_off = LDS_MISC) {
;     ...
;     for (;;) {
;         __syncthreads();
;         if (tid == 0) *slot = first + (int)atomicAdd(&p.ctl[cw], 1u);
;         __syncthreads();
;         const int it = *slot;
;         if (it >= last) break;
.LBB0_1276:
	s_or_b64 exec, exec, s[50:51]
	s_waitcnt vmcnt(0)
	v_readfirstlane_b32 s2, v1
	v_mov_b32_e32 v1, s13
	s_nop 0
	v_add_u32_e32 v0, s2, v0
	v_add_u32_e32 v0, 0x460, v0
	ds_write_b32 v1, v0
